# all global stores write-through (sc1) and buffer_wbl2 removed from the 14 grid barriers; early invalidate kept
# speedup vs baseline: 1.0152x; 1.0049x over previous
.LBB0_116:
	s_or_b64 exec, exec, s[14:15]
	v_or_b32_e32 v128, s22, v121
	v_ashrrev_i32_e32 v129, 31, v128
	v_lshlrev_b64 v[128:129], 5, v[128:129]
	v_lshl_add_u64 v[128:129], v[102:103], 0, v[128:129]
	global_store_dword v[128:129], v105, off sc1

.LBB0_263:
	s_andn2_saveexec_b64 s[8:9], s[8:9]
	s_cbranch_execz .LBB0_283
	s_mov_b64 s[8:9], exec
	s_waitcnt lgkmcnt(0)
	s_waitcnt vmcnt(0)
	v_mbcnt_lo_u32_b32 v2, s8, 0
	v_mbcnt_hi_u32_b32 v2, s9, v2
	v_cmp_eq_u32_e32 vcc, 0, v2
	s_and_saveexec_b64 s[10:11], vcc
	s_cbranch_execz .LBB0_266
	s_bcnt1_i32_b64 s8, s[8:9]
	v_mov_b32_e32 v3, 0x7000
	v_mov_b32_e32 v4, s8
	global_atomic_add v3, v3, v4, s[54:55] offset:1024 sc0

.LBB0_288:
	s_waitcnt vmcnt(6)
	v_add_u32_e32 v10, s6, v222
	v_ashrrev_i32_e32 v11, 31, v10
	v_lshlrev_b64 v[10:11], 11, v[10:11]
	v_lshl_add_u64 v[54:55], v[4:5], 0, v[10:11]
	v_add_co_u32_e32 v56, vcc, 0x8000, v54
	global_load_dwordx4 v[10:13], v[54:55], off
	global_load_dwordx4 v[14:17], v[2:3], off
	v_addc_co_u32_e32 v57, vcc, 0, v55, vcc
	v_add_co_u32_e32 v58, vcc, 0x10000, v54
	global_load_dwordx4 v[18:21], v[56:57], off
	s_nop 0
	v_addc_co_u32_e32 v59, vcc, 0, v55, vcc
	v_add_co_u32_e32 v60, vcc, 0x18000, v54
	global_load_dwordx4 v[22:25], v[58:59], off
	s_nop 0
	v_addc_co_u32_e32 v61, vcc, 0, v55, vcc
	global_load_dwordx4 v[26:29], v[60:61], off
	global_load_dwordx4 v[30:33], v[54:55], off offset:64
	global_load_dwordx4 v[34:37], v[2:3], off offset:64
	global_load_dwordx4 v[38:41], v[56:57], off offset:64
	global_load_dwordx4 v[42:45], v[58:59], off offset:64
	global_load_dwordx4 v[46:49], v[60:61], off offset:64
	s_and_b64 vcc, exec, s[4:5]
	s_waitcnt vmcnt(8)
	v_mfma_f32_16x16x32_bf16 v[10:13], v[10:13], v[14:17], 0
	s_waitcnt vmcnt(7)
	v_mfma_f32_16x16x32_bf16 v[18:21], v[18:21], v[14:17], 0
	s_waitcnt vmcnt(6)
	v_mfma_f32_16x16x32_bf16 v[22:25], v[22:25], v[14:17], 0
	s_waitcnt vmcnt(5)
	v_mfma_f32_16x16x32_bf16 v[14:17], v[26:29], v[14:17], 0
	global_load_dwordx4 v[26:29], v[54:55], off offset:128
	global_load_dwordx4 v[50:53], v[2:3], off offset:128
	s_waitcnt vmcnt(5)
	v_mfma_f32_16x16x32_bf16 v[10:13], v[30:33], v[34:37], v[10:13]
	global_load_dwordx4 v[30:33], v[56:57], off offset:128
	s_waitcnt vmcnt(5)
	v_mfma_f32_16x16x32_bf16 v[18:21], v[38:41], v[34:37], v[18:21]
	global_load_dwordx4 v[38:41], v[58:59], off offset:128
	s_waitcnt vmcnt(5)
	v_mfma_f32_16x16x32_bf16 v[22:25], v[42:45], v[34:37], v[22:25]
	global_load_dwordx4 v[42:45], v[60:61], off offset:128
	s_waitcnt vmcnt(5)
	v_mfma_f32_16x16x32_bf16 v[14:17], v[46:49], v[34:37], v[14:17]
	global_load_dwordx4 v[34:37], v[54:55], off offset:192
	global_load_dwordx4 v[46:49], v[2:3], off offset:192
	s_waitcnt vmcnt(5)
	v_mfma_f32_16x16x32_bf16 v[10:13], v[26:29], v[50:53], v[10:13]
	global_load_dwordx4 v[26:29], v[56:57], off offset:192
	s_waitcnt vmcnt(5)
	v_mfma_f32_16x16x32_bf16 v[18:21], v[30:33], v[50:53], v[18:21]
	global_load_dwordx4 v[30:33], v[58:59], off offset:192
	s_waitcnt vmcnt(5)
	v_mfma_f32_16x16x32_bf16 v[22:25], v[38:41], v[50:53], v[22:25]
	global_load_dwordx4 v[38:41], v[60:61], off offset:192
	s_barrier
	s_waitcnt vmcnt(5)
	v_mfma_f32_16x16x32_bf16 v[14:17], v[42:45], v[50:53], v[14:17]
	s_waitcnt vmcnt(3)
	v_mfma_f32_16x16x32_bf16 v[10:13], v[34:37], v[46:49], v[10:13]
	s_waitcnt vmcnt(2)
	v_mfma_f32_16x16x32_bf16 v[18:21], v[26:29], v[46:49], v[18:21]
	s_waitcnt vmcnt(1)
	v_mfma_f32_16x16x32_bf16 v[22:25], v[30:33], v[46:49], v[22:25]
	s_waitcnt vmcnt(0)
	v_mfma_f32_16x16x32_bf16 v[14:17], v[38:41], v[46:49], v[14:17]
	s_nop 1
	ds_write_b128 v8, v[10:13]
	s_nop 0
	ds_write_b128 v8, v[18:21] offset:1024
	s_nop 0
	ds_write_b128 v8, v[22:25] offset:2048
	s_nop 0
	ds_write_b128 v8, v[14:17] offset:3072
	s_waitcnt lgkmcnt(0)
	s_barrier
	s_cbranch_vccnz .LBB0_287
	ds_read_b128 v[10:13], v1
	ds_read_b128 v[14:17], v1 offset:4096
	ds_read_b128 v[18:21], v1 offset:8192
	ds_read_b128 v[22:25], v1 offset:1024
	ds_read_b128 v[26:29], v1 offset:5120
	s_cmp_lt_i32 s11, 8
	s_waitcnt lgkmcnt(3)
	v_pk_add_f32 v[30:31], v[12:13], v[16:17]
	v_pk_add_f32 v[32:33], v[10:11], v[14:15]
	ds_read_b128 v[10:13], v1 offset:12288
	ds_read_b128 v[14:17], v1 offset:9216
	s_waitcnt lgkmcnt(4)
	v_pk_add_f32 v[34:35], v[30:31], v[20:21]
	v_pk_add_f32 v[36:37], v[32:33], v[18:19]
	ds_read_b128 v[18:21], v1 offset:16384
	ds_read_b128 v[30:33], v1 offset:13312
	s_waitcnt lgkmcnt(3)
	v_pk_add_f32 v[38:39], v[34:35], v[12:13]
	v_pk_add_f32 v[40:41], v[36:37], v[10:11]
	ds_read_b128 v[10:13], v1 offset:20480
	ds_read_b128 v[34:37], v1 offset:17408
	s_waitcnt lgkmcnt(3)
	v_pk_add_f32 v[42:43], v[38:39], v[20:21]
	v_pk_add_f32 v[44:45], v[40:41], v[18:19]
	ds_read_b128 v[18:21], v1 offset:24576
	ds_read_b128 v[38:41], v1 offset:21504
	s_waitcnt lgkmcnt(3)
	v_pk_add_f32 v[46:47], v[42:43], v[12:13]
	v_pk_add_f32 v[48:49], v[44:45], v[10:11]
	ds_read_b128 v[10:13], v1 offset:28672
	ds_read_b128 v[42:45], v1 offset:25600
	s_waitcnt lgkmcnt(3)
	v_pk_add_f32 v[48:49], v[48:49], v[18:19]
	v_pk_add_f32 v[46:47], v[46:47], v[20:21]
	ds_read_b128 v[18:21], v1 offset:29696
	s_waitcnt lgkmcnt(2)
	v_pk_add_f32 v[48:49], v[48:49], v[10:11]
	v_pk_add_f32 v[10:11], v[24:25], v[28:29]
	v_pk_add_f32 v[46:47], v[46:47], v[12:13]
	v_pk_add_f32 v[12:13], v[22:23], v[26:27]
	v_pk_add_f32 v[10:11], v[10:11], v[16:17]
	v_pk_add_f32 v[12:13], v[12:13], v[14:15]
	v_pk_add_f32 v[10:11], v[10:11], v[32:33]
	v_pk_add_f32 v[12:13], v[12:13], v[30:31]
	v_pk_add_f32 v[10:11], v[10:11], v[36:37]
	v_pk_add_f32 v[12:13], v[12:13], v[34:35]
	v_pk_add_f32 v[10:11], v[10:11], v[40:41]
	v_pk_add_f32 v[12:13], v[12:13], v[38:39]
	s_waitcnt lgkmcnt(1)
	v_pk_add_f32 v[10:11], v[10:11], v[44:45]
	v_pk_add_f32 v[22:23], v[12:13], v[42:43]
	s_waitcnt lgkmcnt(0)
	v_pk_add_f32 v[50:51], v[10:11], v[20:21]
	ds_read_b128 v[10:13], v1 offset:2048
	ds_read_b128 v[14:17], v1 offset:6144
	v_pk_add_f32 v[52:53], v[22:23], v[18:19]
	ds_read_b128 v[18:21], v1 offset:10240
	ds_read_b128 v[22:25], v1 offset:3072
	ds_read_b128 v[26:29], v1 offset:7168
	s_cselect_b64 vcc, -1, 0
	s_ashr_i32 s7, s6, 31
	s_waitcnt lgkmcnt(3)
	v_pk_add_f32 v[30:31], v[12:13], v[16:17]
	v_pk_add_f32 v[32:33], v[10:11], v[14:15]
	ds_read_b128 v[10:13], v1 offset:14336
	ds_read_b128 v[14:17], v1 offset:11264
	s_waitcnt lgkmcnt(4)
	v_pk_add_f32 v[34:35], v[30:31], v[20:21]
	v_pk_add_f32 v[36:37], v[32:33], v[18:19]
	ds_read_b128 v[18:21], v1 offset:18432
	ds_read_b128 v[30:33], v1 offset:15360
	s_waitcnt lgkmcnt(3)
	v_pk_add_f32 v[38:39], v[34:35], v[12:13]
	v_pk_add_f32 v[40:41], v[36:37], v[10:11]
	ds_read_b128 v[10:13], v1 offset:22528
	ds_read_b128 v[34:37], v1 offset:19456
	s_waitcnt lgkmcnt(3)
	v_pk_add_f32 v[42:43], v[38:39], v[20:21]
	v_pk_add_f32 v[44:45], v[40:41], v[18:19]
	ds_read_b128 v[18:21], v1 offset:26624
	ds_read_b128 v[38:41], v1 offset:23552
	s_waitcnt lgkmcnt(3)
	v_pk_add_f32 v[54:55], v[42:43], v[12:13]
	v_pk_add_f32 v[56:57], v[44:45], v[10:11]
	ds_read_b128 v[10:13], v1 offset:30720
	ds_read_b128 v[42:45], v1 offset:27648
	v_pk_add_f32 v[22:23], v[22:23], v[26:27]
	s_waitcnt lgkmcnt(3)
	v_pk_add_f32 v[54:55], v[54:55], v[20:21]
	v_pk_add_f32 v[56:57], v[56:57], v[18:19]
	ds_read_b128 v[18:21], v1 offset:31744
	v_pk_add_f32 v[14:15], v[22:23], v[14:15]
	v_pk_add_f32 v[24:25], v[24:25], v[28:29]
	v_pk_add_f32 v[14:15], v[14:15], v[30:31]
	v_pk_add_f32 v[16:17], v[24:25], v[16:17]
	v_pk_add_f32 v[14:15], v[14:15], v[34:35]
	v_pk_add_f32 v[16:17], v[16:17], v[32:33]
	s_waitcnt lgkmcnt(3)
	v_pk_add_f32 v[14:15], v[14:15], v[38:39]
	v_pk_add_f32 v[16:17], v[16:17], v[36:37]
	s_waitcnt lgkmcnt(1)
	v_pk_add_f32 v[14:15], v[14:15], v[42:43]
	v_pk_add_f32 v[16:17], v[16:17], v[40:41]
	s_waitcnt lgkmcnt(0)
	v_pk_add_f32 v[14:15], v[14:15], v[18:19]
	v_cndmask_b32_e32 v18, 1.0, v9, vcc
	v_pk_mul_f32 v[24:25], v[18:19], v[48:49] op_sel_hi:[0,1]
	v_pk_mul_f32 v[22:23], v[18:19], v[46:47] op_sel_hi:[0,1]
	v_bfe_u32 v19, v24, 16, 1
	v_add3_u32 v19, v24, v19, s9
	v_bfe_u32 v24, v25, 16, 1
	v_lshrrev_b32_e32 v19, 16, v19
	v_add3_u32 v24, v25, v24, s9
	v_and_or_b32 v24, v24, s10, v19
	v_bfe_u32 v19, v22, 16, 1
	v_add3_u32 v19, v22, v19, s9
	v_bfe_u32 v22, v23, 16, 1
	v_pk_add_f32 v[16:17], v[16:17], v[44:45]
	v_lshrrev_b32_e32 v19, 16, v19
	v_add3_u32 v22, v23, v22, s9
	v_pk_add_f32 v[16:17], v[16:17], v[20:21]
	v_lshl_add_u64 v[20:21], s[6:7], 1, v[6:7]
	v_and_or_b32 v25, v22, s10, v19
	global_store_dwordx2 v[20:21], v[24:25], off sc1
	v_pk_mul_f32 v[24:25], v[18:19], v[52:53] op_sel_hi:[0,1]
	v_pk_mul_f32 v[22:23], v[18:19], v[50:51] op_sel_hi:[0,1]
	v_bfe_u32 v19, v24, 16, 1
	v_add3_u32 v19, v24, v19, s9
	v_bfe_u32 v24, v25, 16, 1
	v_lshrrev_b32_e32 v19, 16, v19
	v_add3_u32 v24, v25, v24, s9
	v_and_or_b32 v24, v24, s10, v19
	v_bfe_u32 v19, v22, 16, 1
	v_add3_u32 v19, v22, v19, s9
	v_pk_add_f32 v[10:11], v[56:57], v[10:11]
	v_lshrrev_b32_e32 v19, 16, v19
	v_bfe_u32 v22, v23, 16, 1
	v_pk_add_f32 v[12:13], v[54:55], v[12:13]
	v_add3_u32 v22, v23, v22, s9
	v_pk_mul_f32 v[10:11], v[18:19], v[10:11] op_sel_hi:[0,1]
	v_and_or_b32 v25, v22, s10, v19
	v_pk_mul_f32 v[12:13], v[18:19], v[12:13] op_sel_hi:[0,1]
	v_bfe_u32 v19, v10, 16, 1
	v_add3_u32 v10, v10, v19, s9
	v_bfe_u32 v19, v11, 16, 1
	v_lshrrev_b32_e32 v10, 16, v10
	v_add3_u32 v11, v11, v19, s9
	v_and_or_b32 v10, v11, s10, v10
	v_bfe_u32 v11, v12, 16, 1
	v_add3_u32 v11, v12, v11, s9
	v_bfe_u32 v12, v13, 16, 1
	v_lshrrev_b32_e32 v11, 16, v11
	v_add3_u32 v12, v13, v12, s9
	v_and_or_b32 v11, v12, s10, v11
	v_pk_mul_f32 v[12:13], v[18:19], v[14:15] op_sel_hi:[0,1]
	v_bfe_u32 v14, v12, 16, 1
	v_add3_u32 v12, v12, v14, s9
	v_bfe_u32 v14, v13, 16, 1
	global_store_dwordx2 v[20:21], v[10:11], off offset:64 sc1
	v_pk_mul_f32 v[10:11], v[18:19], v[16:17] op_sel_hi:[0,1]
	v_lshrrev_b32_e32 v12, 16, v12
	v_add3_u32 v13, v13, v14, s9
	v_and_or_b32 v12, v13, s10, v12
	v_bfe_u32 v13, v10, 16, 1
	v_add3_u32 v10, v10, v13, s9
	v_bfe_u32 v13, v11, 16, 1
	v_lshrrev_b32_e32 v10, 16, v10
	v_add3_u32 v11, v11, v13, s9
	v_and_or_b32 v13, v11, s10, v10
	global_store_dwordx2 v[20:21], v[24:25], off offset:32 sc1
	global_store_dwordx2 v[20:21], v[12:13], off offset:96 sc1
	s_branch .LBB0_287

.LBB0_404:
	s_or_b64 exec, exec, s[64:65]
	s_and_saveexec_b64 s[26:27], s[78:79]
	s_cbranch_execz .LBB0_406
	s_ashr_i32 s61, s60, 31
	s_lshl_b64 s[64:65], s[60:61], 2
	s_add_u32 s64, s0, s64
	s_addc_u32 s65, s1, s65
	s_waitcnt lgkmcnt(0)
	global_store_dword v6, v7, s[64:65] sc1

.LBB0_424:
	s_waitcnt vmcnt(0)
	v_bfe_u32 v2, v98, 16, 1
	v_add3_u32 v2, v98, v2, s73
	ds_write_b16_d16_hi v128, v2 offset:55296
	v_bfe_u32 v2, v99, 16, 1
	v_add3_u32 v2, v99, v2, s73
	ds_write_b16_d16_hi v128, v2 offset:55840
	v_bfe_u32 v2, v100, 16, 1
	v_add3_u32 v2, v100, v2, s73
	ds_write_b16_d16_hi v128, v2 offset:56384
	v_bfe_u32 v2, v101, 16, 1
	v_add3_u32 v2, v101, v2, s73
	ds_write_b16_d16_hi v142, v2 offset:55296
	v_bfe_u32 v2, v94, 16, 1
	v_add3_u32 v2, v94, v2, s73
	ds_write_b16_d16_hi v128, v2 offset:55328
	v_bfe_u32 v2, v95, 16, 1
	v_add3_u32 v2, v95, v2, s73
	ds_write_b16_d16_hi v128, v2 offset:55872
	v_bfe_u32 v2, v96, 16, 1
	v_add3_u32 v2, v96, v2, s73
	ds_write_b16_d16_hi v128, v2 offset:56416
	v_bfe_u32 v2, v97, 16, 1
	v_add3_u32 v2, v97, v2, s73
	ds_write_b16_d16_hi v142, v2 offset:55328
	v_bfe_u32 v2, v90, 16, 1
	v_add3_u32 v2, v90, v2, s73
	ds_write_b16_d16_hi v128, v2 offset:55360
	v_bfe_u32 v2, v91, 16, 1
	v_add3_u32 v2, v91, v2, s73
	ds_write_b16_d16_hi v128, v2 offset:55904
	v_bfe_u32 v2, v92, 16, 1
	v_add3_u32 v2, v92, v2, s73
	ds_write_b16_d16_hi v128, v2 offset:56448
	v_bfe_u32 v2, v93, 16, 1
	v_add3_u32 v2, v93, v2, s73
	ds_write_b16_d16_hi v142, v2 offset:55360
	v_bfe_u32 v2, v86, 16, 1
	v_add3_u32 v2, v86, v2, s73
	ds_write_b16_d16_hi v128, v2 offset:55392
	v_bfe_u32 v2, v87, 16, 1
	v_add3_u32 v2, v87, v2, s73
	ds_write_b16_d16_hi v128, v2 offset:55936
	v_bfe_u32 v2, v88, 16, 1
	v_add3_u32 v2, v88, v2, s73
	ds_write_b16_d16_hi v128, v2 offset:56480
	v_bfe_u32 v2, v89, 16, 1
	v_add3_u32 v2, v89, v2, s73
	ds_write_b16_d16_hi v142, v2 offset:55392
	v_bfe_u32 v2, v82, 16, 1
	v_add3_u32 v2, v82, v2, s73
	ds_write_b16_d16_hi v128, v2 offset:55424
	v_bfe_u32 v2, v83, 16, 1
	v_add3_u32 v2, v83, v2, s73
	ds_write_b16_d16_hi v128, v2 offset:55968
	v_bfe_u32 v2, v84, 16, 1
	v_add3_u32 v2, v84, v2, s73
	ds_write_b16_d16_hi v128, v2 offset:56512
	v_bfe_u32 v2, v85, 16, 1
	v_add3_u32 v2, v85, v2, s73
	ds_write_b16_d16_hi v142, v2 offset:55424
	v_bfe_u32 v2, v78, 16, 1
	v_add3_u32 v2, v78, v2, s73
	ds_write_b16_d16_hi v128, v2 offset:55456
	v_bfe_u32 v2, v79, 16, 1
	v_add3_u32 v2, v79, v2, s73
	ds_write_b16_d16_hi v128, v2 offset:56000
	v_bfe_u32 v2, v80, 16, 1
	v_add3_u32 v2, v80, v2, s73
	ds_write_b16_d16_hi v128, v2 offset:56544
	v_bfe_u32 v2, v81, 16, 1
	v_add3_u32 v2, v81, v2, s73
	ds_write_b16_d16_hi v142, v2 offset:55456
	v_bfe_u32 v2, v74, 16, 1
	v_add3_u32 v2, v74, v2, s73
	ds_write_b16_d16_hi v128, v2 offset:55488
	v_bfe_u32 v2, v75, 16, 1
	v_add3_u32 v2, v75, v2, s73
	ds_write_b16_d16_hi v128, v2 offset:56032
	v_bfe_u32 v2, v76, 16, 1
	v_add3_u32 v2, v76, v2, s73
	ds_write_b16_d16_hi v128, v2 offset:56576
	v_bfe_u32 v2, v77, 16, 1
	v_add3_u32 v2, v77, v2, s73
	ds_write_b16_d16_hi v142, v2 offset:55488
	v_bfe_u32 v2, v70, 16, 1
	v_add3_u32 v2, v70, v2, s73
	ds_write_b16_d16_hi v128, v2 offset:55520
	v_bfe_u32 v2, v71, 16, 1
	v_add3_u32 v2, v71, v2, s73
	ds_write_b16_d16_hi v128, v2 offset:56064
	v_bfe_u32 v2, v72, 16, 1
	v_add3_u32 v2, v72, v2, s73
	ds_write_b16_d16_hi v128, v2 offset:56608
	v_bfe_u32 v2, v73, 16, 1
	v_add3_u32 v2, v73, v2, s73
	ds_write_b16_d16_hi v142, v2 offset:55520
	v_bfe_u32 v2, v66, 16, 1
	v_add3_u32 v2, v66, v2, s73
	ds_write_b16_d16_hi v128, v2 offset:55552
	v_bfe_u32 v2, v67, 16, 1
	v_add3_u32 v2, v67, v2, s73
	ds_write_b16_d16_hi v128, v2 offset:56096
	v_bfe_u32 v2, v68, 16, 1
	v_add3_u32 v2, v68, v2, s73
	ds_write_b16_d16_hi v128, v2 offset:56640
	v_bfe_u32 v2, v69, 16, 1
	v_add3_u32 v2, v69, v2, s73
	ds_write_b16_d16_hi v142, v2 offset:55552
	v_bfe_u32 v2, v62, 16, 1
	v_add3_u32 v2, v62, v2, s73
	ds_write_b16_d16_hi v128, v2 offset:55584
	v_bfe_u32 v2, v63, 16, 1
	v_add3_u32 v2, v63, v2, s73
	ds_write_b16_d16_hi v128, v2 offset:56128
	v_bfe_u32 v2, v64, 16, 1
	v_add3_u32 v2, v64, v2, s73
	ds_write_b16_d16_hi v128, v2 offset:56672
	v_bfe_u32 v2, v65, 16, 1
	v_add3_u32 v2, v65, v2, s73
	ds_write_b16_d16_hi v142, v2 offset:55584
	v_bfe_u32 v2, v58, 16, 1
	v_add3_u32 v2, v58, v2, s73
	ds_write_b16_d16_hi v128, v2 offset:55616
	v_bfe_u32 v2, v59, 16, 1
	v_add3_u32 v2, v59, v2, s73
	ds_write_b16_d16_hi v128, v2 offset:56160
	v_bfe_u32 v2, v60, 16, 1
	v_add3_u32 v2, v60, v2, s73
	ds_write_b16_d16_hi v128, v2 offset:56704
	v_bfe_u32 v2, v61, 16, 1
	v_add3_u32 v2, v61, v2, s73
	ds_write_b16_d16_hi v142, v2 offset:55616
	v_bfe_u32 v2, v54, 16, 1
	v_add3_u32 v2, v54, v2, s73
	ds_write_b16_d16_hi v128, v2 offset:55648
	v_bfe_u32 v2, v55, 16, 1
	v_add3_u32 v2, v55, v2, s73
	ds_write_b16_d16_hi v128, v2 offset:56192
	v_bfe_u32 v2, v56, 16, 1
	v_add3_u32 v2, v56, v2, s73
	ds_write_b16_d16_hi v128, v2 offset:56736
	v_bfe_u32 v2, v57, 16, 1
	v_add3_u32 v2, v57, v2, s73
	ds_write_b16_d16_hi v142, v2 offset:55648
	v_bfe_u32 v2, v46, 16, 1
	v_add3_u32 v2, v46, v2, s73
	ds_write_b16_d16_hi v128, v2 offset:55680
	v_bfe_u32 v2, v47, 16, 1
	v_add3_u32 v2, v47, v2, s73
	ds_write_b16_d16_hi v128, v2 offset:56224
	v_bfe_u32 v2, v48, 16, 1
	v_add3_u32 v2, v48, v2, s73
	ds_write_b16_d16_hi v128, v2 offset:56768
	v_bfe_u32 v2, v49, 16, 1
	v_add3_u32 v2, v49, v2, s73
	ds_write_b16_d16_hi v142, v2 offset:55680
	v_bfe_u32 v2, v42, 16, 1
	v_add3_u32 v2, v42, v2, s73
	ds_write_b16_d16_hi v128, v2 offset:55712
	v_bfe_u32 v2, v43, 16, 1
	v_add3_u32 v2, v43, v2, s73
	ds_write_b16_d16_hi v128, v2 offset:56256
	v_bfe_u32 v2, v44, 16, 1
	v_add3_u32 v2, v44, v2, s73
	ds_write_b16_d16_hi v128, v2 offset:56800
	v_bfe_u32 v2, v45, 16, 1
	v_add3_u32 v2, v45, v2, s73
	ds_write_b16_d16_hi v142, v2 offset:55712
	v_bfe_u32 v2, v38, 16, 1
	v_add3_u32 v2, v38, v2, s73
	ds_write_b16_d16_hi v128, v2 offset:55744
	v_bfe_u32 v2, v39, 16, 1
	v_add3_u32 v2, v39, v2, s73
	ds_write_b16_d16_hi v128, v2 offset:56288
	v_bfe_u32 v2, v40, 16, 1
	v_add3_u32 v2, v40, v2, s73
	ds_write_b16_d16_hi v128, v2 offset:56832
	v_bfe_u32 v2, v41, 16, 1
	v_add3_u32 v2, v41, v2, s73
	ds_write_b16_d16_hi v142, v2 offset:55744
	v_bfe_u32 v2, v34, 16, 1
	v_add3_u32 v2, v34, v2, s73
	ds_write_b16_d16_hi v128, v2 offset:55776
	v_bfe_u32 v2, v35, 16, 1
	v_add3_u32 v2, v35, v2, s73
	ds_write_b16_d16_hi v128, v2 offset:56320
	v_bfe_u32 v2, v36, 16, 1
	v_add3_u32 v2, v36, v2, s73
	ds_write_b16_d16_hi v128, v2 offset:56864
	v_bfe_u32 v2, v37, 16, 1
	v_add3_u32 v2, v37, v2, s73
	ds_write_b16_d16_hi v142, v2 offset:55776
	v_bfe_u32 v2, v50, 16, 1
	v_add3_u32 v2, v50, v2, s73
	ds_write_b16_d16_hi v128, v2 offset:55808
	v_bfe_u32 v2, v51, 16, 1
	v_add3_u32 v2, v51, v2, s73
	ds_write_b16_d16_hi v128, v2 offset:56352
	v_bfe_u32 v2, v52, 16, 1
	v_add3_u32 v2, v52, v2, s73
	ds_write_b16_d16_hi v128, v2 offset:56896
	v_bfe_u32 v2, v53, 16, 1
	v_add3_u32 v2, v53, v2, s73
	ds_write_b16_d16_hi v142, v2 offset:55808
	ds_read_b128 v[2:5], v144 offset:55296
	s_mul_i32 s26, s60, 0x11000
	s_mul_hi_i32 s27, s60, 0x11000
	s_add_u32 s26, s69, s26
	s_addc_u32 s27, s70, s27
	s_waitcnt lgkmcnt(0)
	global_store_dwordx4 v143, v[2:5], s[26:27] sc1
	ds_read_b128 v[2:5], v146 offset:55296
	s_waitcnt lgkmcnt(0)
	global_store_dwordx4 v145, v[2:5], s[26:27] sc1
	ds_read_b128 v[2:5], v148 offset:55296
	s_waitcnt lgkmcnt(0)
	global_store_dwordx4 v147, v[2:5], s[26:27] sc1
	ds_read_b128 v[2:5], v150 offset:55296
	s_waitcnt lgkmcnt(0)
	global_store_dwordx4 v149, v[2:5], s[26:27] sc1
	ds_read_b128 v[2:5], v152 offset:55296
	s_waitcnt lgkmcnt(0)
	global_store_dwordx4 v151, v[2:5], s[26:27] sc1
	ds_read_b128 v[2:5], v154 offset:55296
	s_waitcnt lgkmcnt(0)
	global_store_dwordx4 v153, v[2:5], s[26:27] sc1
	ds_read_b128 v[2:5], v156 offset:55296
	s_waitcnt lgkmcnt(0)
	global_store_dwordx4 v155, v[2:5], s[26:27] sc1
	ds_read_b128 v[2:5], v159 offset:55296
	s_waitcnt lgkmcnt(0)
	global_store_dwordx4 v157, v[2:5], s[26:27] sc1
	s_and_saveexec_b64 s[60:61], s[24:25]
	s_cbranch_execz .LBB0_362
	ds_read_b128 v[2:5], v161 offset:55296
	s_waitcnt lgkmcnt(0)
	global_store_dwordx4 v160, v[2:5], s[26:27] sc1
	s_branch .LBB0_362

.LBB0_460:
	s_andn2_saveexec_b64 s[10:11], s[10:11]
	s_cbranch_execz .LBB0_480
	s_mov_b64 s[10:11], exec
	s_waitcnt lgkmcnt(0)
	s_waitcnt vmcnt(0)
	v_mbcnt_lo_u32_b32 v2, s10, 0
	v_mbcnt_hi_u32_b32 v2, s11, v2
	v_cmp_eq_u32_e32 vcc, 0, v2
	s_and_saveexec_b64 s[12:13], vcc
	s_cbranch_execz .LBB0_463
	s_bcnt1_i32_b64 s10, s[10:11]
	v_mov_b32_e32 v3, 0x7000
	v_mov_b32_e32 v4, s10
	global_atomic_add v3, v3, v4, s[54:55] offset:1024 sc0

.LBB0_485:
	s_cmp_eq_u32 s13, 0
	s_cselect_b64 vcc, -1, 0
	v_add_u32_e32 v6, s13, v23
	v_cndmask_b32_e32 v6, v6, v22, vcc
	v_ashrrev_i32_e32 v7, 31, v6
	v_mad_i64_i32 v[8:9], s[14:15], v6, s8, v[14:15]
	v_lshl_add_u64 v[6:7], v[6:7], 2, s[0:1]
	global_load_dwordx2 v[8:9], v[8:9], off
	v_lshl_add_u64 v[20:21], s[54:55], 0, v[16:17]
	global_load_dword v6, v[6:7], off
	s_mov_b32 s14, 0x9d00000
	s_add_i32 s13, s13, 16
	s_cmp_eq_u32 s13, 32
	s_waitcnt vmcnt(1)
	v_lshlrev_b32_e32 v10, 16, v8
	v_and_b32_e32 v11, 0xffff0000, v8
	s_waitcnt vmcnt(0)
	v_mul_f32_e32 v6, 0x3fb8aa3b, v6
	v_exp_f32_e32 v6, v6
	v_lshlrev_b32_e32 v8, 16, v9
	v_and_b32_e32 v9, 0xffff0000, v9
	v_pk_fma_f32 v[30:31], v[2:3], v[6:7], v[10:11] op_sel_hi:[1,0,1]
	s_nop 0
	v_bfe_u32 v2, v30, 16, 1
	v_add3_u32 v2, v30, v2, s12
	v_bfe_u32 v3, v31, 16, 1
	v_pk_fma_f32 v[28:29], v[4:5], v[6:7], v[8:9] op_sel_hi:[1,0,1]
	v_lshrrev_b32_e32 v2, 16, v2
	v_add3_u32 v3, v31, v3, s12
	v_and_or_b32 v2, v3, s11, v2
	v_bfe_u32 v3, v28, 16, 1
	v_add3_u32 v3, v28, v3, s12
	v_bfe_u32 v4, v29, 16, 1
	v_lshrrev_b32_e32 v3, 16, v3
	v_add3_u32 v4, v29, v4, s12
	v_and_or_b32 v3, v4, s11, v3
	v_add_co_u32_e32 v4, vcc, s14, v20
	s_mov_b32 s14, 0xae80000
	s_nop 0
	v_addc_co_u32_e32 v5, vcc, 0, v21, vcc
	global_store_dwordx2 v[4:5], v[2:3], off sc1
	v_add_co_u32_e32 v2, vcc, s14, v20
	s_mov_b64 s[14:15], 0x1400000
	s_nop 0
	v_addc_co_u32_e32 v3, vcc, 0, v21, vcc
	global_load_dwordx2 v[2:3], v[2:3], off
	s_waitcnt vmcnt(0)
	v_lshlrev_b32_e32 v32, 16, v2
	v_and_b32_e32 v33, 0xffff0000, v2
	v_lshlrev_b32_e32 v34, 16, v3
	v_and_b32_e32 v35, 0xffff0000, v3
	v_lshl_add_u64 v[2:3], s[54:55], 0, v[18:19]
	v_lshl_add_u64 v[6:7], v[2:3], 0, s[14:15]
	s_mov_b32 s14, 0x1400000
	v_add_co_u32_e32 v2, vcc, s14, v2
	s_mov_b32 s14, 0x9d11000
	s_nop 0
	v_addc_co_u32_e32 v3, vcc, 0, v3, vcc
	global_load_dwordx4 v[24:27], v[2:3], off
	global_load_dwordx3 v[10:12], v[6:7], off offset:48
	s_nop 0
	global_load_dwordx4 v[2:5], v[6:7], off offset:32
	s_nop 0
	global_load_dwordx4 v[6:9], v[6:7], off offset:16
	v_lshl_add_u64 v[18:19], v[18:19], 0, 64
	s_waitcnt vmcnt(3)
	v_mul_f32_e32 v24, 0x3fb8aa3b, v24
	v_exp_f32_e32 v24, v24
	v_mul_f32_e32 v26, 0x3fb8aa3b, v26
	v_exp_f32_e32 v26, v26
	s_waitcnt vmcnt(0)
	v_mul_f32_e32 v6, 0x3fb8aa3b, v6
	v_pk_fma_f32 v[30:31], v[30:31], v[24:25], v[32:33] op_sel_hi:[1,0,1]
	v_pk_fma_f32 v[28:29], v[28:29], v[24:25], v[34:35] op_sel_hi:[1,0,1]
	v_bfe_u32 v24, v30, 16, 1
	v_add3_u32 v24, v30, v24, s12
	v_bfe_u32 v32, v31, 16, 1
	v_lshrrev_b32_e32 v24, 16, v24
	v_add3_u32 v32, v31, v32, s12
	v_and_or_b32 v32, v32, s11, v24
	v_bfe_u32 v24, v28, 16, 1
	v_add3_u32 v24, v28, v24, s12
	v_bfe_u32 v33, v29, 16, 1
	v_lshrrev_b32_e32 v24, 16, v24
	v_add3_u32 v33, v29, v33, s12
	v_add_co_u32_e32 v34, vcc, s14, v20
	v_and_or_b32 v33, v33, s11, v24
	s_nop 0
	v_addc_co_u32_e32 v35, vcc, 0, v21, vcc
	s_mov_b32 s14, 0xae91000
	global_store_dwordx2 v[34:35], v[32:33], off sc1
	v_add_co_u32_e32 v32, vcc, s14, v20
	v_mul_f32_e32 v24, 0x3fb8aa3b, v25
	s_nop 0
	v_addc_co_u32_e32 v33, vcc, 0, v21, vcc
	global_load_dwordx2 v[32:33], v[32:33], off
	v_exp_f32_e32 v24, v24
	s_mov_b32 s14, 0x9d22000
	v_exp_f32_e32 v6, v6
	v_mul_f32_e32 v8, 0x3fb8aa3b, v8
	v_exp_f32_e32 v8, v8
	v_mul_f32_e32 v2, 0x3fb8aa3b, v2
	v_exp_f32_e32 v2, v2
	v_mul_f32_e32 v4, 0x3fb8aa3b, v4
	v_exp_f32_e32 v4, v4
	v_mul_f32_e32 v10, 0x3fb8aa3b, v10
	v_exp_f32_e32 v10, v10
	s_waitcnt vmcnt(0)
	v_lshlrev_b32_e32 v34, 16, v32
	v_and_b32_e32 v35, 0xffff0000, v32
	v_lshlrev_b32_e32 v32, 16, v33
	v_and_b32_e32 v33, 0xffff0000, v33
	v_pk_fma_f32 v[28:29], v[28:29], v[24:25], v[32:33] op_sel_hi:[1,0,1]
	v_pk_fma_f32 v[24:25], v[30:31], v[24:25], v[34:35] op_sel_hi:[1,0,1]
	v_bfe_u32 v32, v29, 16, 1
	v_bfe_u32 v30, v24, 16, 1
	v_add3_u32 v30, v24, v30, s12
	v_bfe_u32 v31, v25, 16, 1
	v_lshrrev_b32_e32 v30, 16, v30
	v_add3_u32 v31, v25, v31, s12
	v_and_or_b32 v30, v31, s11, v30
	v_bfe_u32 v31, v28, 16, 1
	v_add3_u32 v31, v28, v31, s12
	v_lshrrev_b32_e32 v31, 16, v31
	v_add3_u32 v32, v29, v32, s12
	v_and_or_b32 v31, v32, s11, v31
	v_add_co_u32_e32 v32, vcc, s14, v20
	s_mov_b32 s14, 0xaea2000
	s_nop 0
	v_addc_co_u32_e32 v33, vcc, 0, v21, vcc
	global_store_dwordx2 v[32:33], v[30:31], off sc1
	v_add_co_u32_e32 v30, vcc, s14, v20
	s_mov_b32 s14, 0x9d33000
	s_nop 0
	v_addc_co_u32_e32 v31, vcc, 0, v21, vcc
	global_load_dwordx2 v[30:31], v[30:31], off
	s_waitcnt vmcnt(0)
	v_lshlrev_b32_e32 v32, 16, v30
	v_and_b32_e32 v33, 0xffff0000, v30
	v_lshlrev_b32_e32 v30, 16, v31
	v_and_b32_e32 v31, 0xffff0000, v31
	v_pk_fma_f32 v[24:25], v[24:25], v[26:27], v[32:33] op_sel_hi:[1,0,1]
	v_pk_fma_f32 v[28:29], v[28:29], v[26:27], v[30:31] op_sel_hi:[1,0,1]
	v_bfe_u32 v26, v24, 16, 1
	v_add3_u32 v26, v24, v26, s12
	v_bfe_u32 v30, v25, 16, 1
	v_lshrrev_b32_e32 v26, 16, v26
	v_add3_u32 v30, v25, v30, s12
	v_and_or_b32 v30, v30, s11, v26
	v_bfe_u32 v26, v28, 16, 1
	v_add3_u32 v26, v28, v26, s12
	v_bfe_u32 v31, v29, 16, 1
	v_lshrrev_b32_e32 v26, 16, v26
	v_add3_u32 v31, v29, v31, s12
	v_add_co_u32_e32 v32, vcc, s14, v20
	v_and_or_b32 v31, v31, s11, v26
	s_nop 0
	v_addc_co_u32_e32 v33, vcc, 0, v21, vcc
	s_mov_b32 s14, 0xaeb3000
	global_store_dwordx2 v[32:33], v[30:31], off sc1
	v_add_co_u32_e32 v30, vcc, s14, v20
	v_mul_f32_e32 v26, 0x3fb8aa3b, v27
	s_nop 0
	v_addc_co_u32_e32 v31, vcc, 0, v21, vcc
	global_load_dwordx2 v[30:31], v[30:31], off
	v_exp_f32_e32 v26, v26
	s_mov_b32 s14, 0x9d44000
	s_waitcnt vmcnt(0)
	v_lshlrev_b32_e32 v32, 16, v30
	v_and_b32_e32 v33, 0xffff0000, v30
	v_lshlrev_b32_e32 v30, 16, v31
	v_and_b32_e32 v31, 0xffff0000, v31
	v_pk_fma_f32 v[24:25], v[24:25], v[26:27], v[32:33] op_sel_hi:[1,0,1]
	v_pk_fma_f32 v[28:29], v[28:29], v[26:27], v[30:31] op_sel_hi:[1,0,1]
	v_bfe_u32 v26, v24, 16, 1
	v_add3_u32 v26, v24, v26, s12
	v_bfe_u32 v27, v25, 16, 1
	v_lshrrev_b32_e32 v26, 16, v26
	v_add3_u32 v27, v25, v27, s12
	v_and_or_b32 v26, v27, s11, v26
	v_bfe_u32 v27, v28, 16, 1
	v_add3_u32 v27, v28, v27, s12
	v_bfe_u32 v30, v29, 16, 1
	v_lshrrev_b32_e32 v27, 16, v27
	v_add3_u32 v30, v29, v30, s12
	v_and_or_b32 v27, v30, s11, v27
	v_add_co_u32_e32 v30, vcc, s14, v20
	s_mov_b32 s14, 0xaec4000
	s_nop 0
	v_addc_co_u32_e32 v31, vcc, 0, v21, vcc
	global_store_dwordx2 v[30:31], v[26:27], off sc1
	v_add_co_u32_e32 v26, vcc, s14, v20
	s_mov_b32 s14, 0x9d55000
	s_nop 0
	v_addc_co_u32_e32 v27, vcc, 0, v21, vcc
	global_load_dwordx2 v[26:27], v[26:27], off
	s_waitcnt vmcnt(0)
	v_lshlrev_b32_e32 v30, 16, v26
	v_and_b32_e32 v31, 0xffff0000, v26
	v_lshlrev_b32_e32 v26, 16, v27
	v_and_b32_e32 v27, 0xffff0000, v27
	v_pk_fma_f32 v[24:25], v[24:25], v[6:7], v[30:31] op_sel_hi:[1,0,1]
	v_pk_fma_f32 v[26:27], v[28:29], v[6:7], v[26:27] op_sel_hi:[1,0,1]
	v_bfe_u32 v6, v24, 16, 1
	v_add3_u32 v6, v24, v6, s12
	v_bfe_u32 v28, v25, 16, 1
	v_lshrrev_b32_e32 v6, 16, v6
	v_add3_u32 v28, v25, v28, s12
	v_and_or_b32 v28, v28, s11, v6
	v_bfe_u32 v6, v26, 16, 1
	v_add3_u32 v6, v26, v6, s12
	v_bfe_u32 v29, v27, 16, 1
	v_lshrrev_b32_e32 v6, 16, v6
	v_add3_u32 v29, v27, v29, s12
	v_add_co_u32_e32 v30, vcc, s14, v20
	v_and_or_b32 v29, v29, s11, v6
	s_nop 0
	v_addc_co_u32_e32 v31, vcc, 0, v21, vcc
	s_mov_b32 s14, 0xaed5000
	global_store_dwordx2 v[30:31], v[28:29], off sc1
	v_add_co_u32_e32 v28, vcc, s14, v20
	v_mul_f32_e32 v6, 0x3fb8aa3b, v7
	s_nop 0
	v_addc_co_u32_e32 v29, vcc, 0, v21, vcc
	global_load_dwordx2 v[28:29], v[28:29], off
	v_exp_f32_e32 v6, v6
	s_mov_b32 s14, 0x9d66000
	s_waitcnt vmcnt(0)
	v_lshlrev_b32_e32 v30, 16, v28
	v_and_b32_e32 v31, 0xffff0000, v28
	v_lshlrev_b32_e32 v28, 16, v29
	v_and_b32_e32 v29, 0xffff0000, v29
	v_pk_fma_f32 v[26:27], v[26:27], v[6:7], v[28:29] op_sel_hi:[1,0,1]
	v_pk_fma_f32 v[6:7], v[24:25], v[6:7], v[30:31] op_sel_hi:[1,0,1]
	v_bfe_u32 v28, v27, 16, 1
	v_bfe_u32 v24, v6, 16, 1
	v_add3_u32 v24, v6, v24, s12
	v_bfe_u32 v25, v7, 16, 1
	v_lshrrev_b32_e32 v24, 16, v24
	v_add3_u32 v25, v7, v25, s12
	v_and_or_b32 v24, v25, s11, v24
	v_bfe_u32 v25, v26, 16, 1
	v_add3_u32 v25, v26, v25, s12
	v_lshrrev_b32_e32 v25, 16, v25
	v_add3_u32 v28, v27, v28, s12
	v_and_or_b32 v25, v28, s11, v25
	v_add_co_u32_e32 v28, vcc, s14, v20
	s_mov_b32 s14, 0xaee6000
	s_nop 0
	v_addc_co_u32_e32 v29, vcc, 0, v21, vcc
	global_store_dwordx2 v[28:29], v[24:25], off sc1
	v_add_co_u32_e32 v24, vcc, s14, v20
	s_mov_b32 s14, 0x9d77000
	s_nop 0
	v_addc_co_u32_e32 v25, vcc, 0, v21, vcc
	global_load_dwordx2 v[24:25], v[24:25], off
	s_waitcnt vmcnt(0)
	v_lshlrev_b32_e32 v28, 16, v24
	v_and_b32_e32 v29, 0xffff0000, v24
	v_lshlrev_b32_e32 v24, 16, v25
	v_and_b32_e32 v25, 0xffff0000, v25
	v_pk_fma_f32 v[6:7], v[6:7], v[8:9], v[28:29] op_sel_hi:[1,0,1]
	v_pk_fma_f32 v[24:25], v[26:27], v[8:9], v[24:25] op_sel_hi:[1,0,1]
	v_bfe_u32 v8, v6, 16, 1
	v_add3_u32 v8, v6, v8, s12
	v_bfe_u32 v26, v7, 16, 1
	v_lshrrev_b32_e32 v8, 16, v8
	v_add3_u32 v26, v7, v26, s12
	v_and_or_b32 v26, v26, s11, v8
	v_bfe_u32 v8, v24, 16, 1
	v_add3_u32 v8, v24, v8, s12
	v_bfe_u32 v27, v25, 16, 1
	v_lshrrev_b32_e32 v8, 16, v8
	v_add3_u32 v27, v25, v27, s12
	v_add_co_u32_e32 v28, vcc, s14, v20
	v_and_or_b32 v27, v27, s11, v8
	s_nop 0
	v_addc_co_u32_e32 v29, vcc, 0, v21, vcc
	s_mov_b32 s14, 0xaef7000
	global_store_dwordx2 v[28:29], v[26:27], off sc1
	v_add_co_u32_e32 v26, vcc, s14, v20
	v_mul_f32_e32 v8, 0x3fb8aa3b, v9
	s_nop 0
	v_addc_co_u32_e32 v27, vcc, 0, v21, vcc
	global_load_dwordx2 v[26:27], v[26:27], off
	v_exp_f32_e32 v8, v8
	s_mov_b32 s14, 0x9d88000
	s_waitcnt vmcnt(0)
	v_lshlrev_b32_e32 v28, 16, v26
	v_and_b32_e32 v29, 0xffff0000, v26
	v_lshlrev_b32_e32 v26, 16, v27
	v_and_b32_e32 v27, 0xffff0000, v27
	v_pk_fma_f32 v[6:7], v[6:7], v[8:9], v[28:29] op_sel_hi:[1,0,1]
	v_pk_fma_f32 v[24:25], v[24:25], v[8:9], v[26:27] op_sel_hi:[1,0,1]
	v_bfe_u32 v8, v6, 16, 1
	v_add3_u32 v8, v6, v8, s12
	v_bfe_u32 v9, v7, 16, 1
	v_lshrrev_b32_e32 v8, 16, v8
	v_add3_u32 v9, v7, v9, s12
	v_and_or_b32 v8, v9, s11, v8
	v_bfe_u32 v9, v24, 16, 1
	v_add3_u32 v9, v24, v9, s12
	v_bfe_u32 v26, v25, 16, 1
	v_lshrrev_b32_e32 v9, 16, v9
	v_add3_u32 v26, v25, v26, s12
	v_and_or_b32 v9, v26, s11, v9
	v_add_co_u32_e32 v26, vcc, s14, v20
	s_mov_b32 s14, 0xaf08000
	s_nop 0
	v_addc_co_u32_e32 v27, vcc, 0, v21, vcc
	global_store_dwordx2 v[26:27], v[8:9], off sc1
	v_add_co_u32_e32 v8, vcc, s14, v20
	s_mov_b32 s14, 0x9d99000
	s_nop 0
	v_addc_co_u32_e32 v9, vcc, 0, v21, vcc
	global_load_dwordx2 v[8:9], v[8:9], off
	s_waitcnt vmcnt(0)
	v_lshlrev_b32_e32 v26, 16, v8
	v_and_b32_e32 v27, 0xffff0000, v8
	v_lshlrev_b32_e32 v8, 16, v9
	v_and_b32_e32 v9, 0xffff0000, v9
	v_pk_fma_f32 v[6:7], v[6:7], v[2:3], v[26:27] op_sel_hi:[1,0,1]
	v_pk_fma_f32 v[8:9], v[24:25], v[2:3], v[8:9] op_sel_hi:[1,0,1]
	v_bfe_u32 v2, v6, 16, 1
	v_add3_u32 v2, v6, v2, s12
	v_bfe_u32 v24, v7, 16, 1
	v_lshrrev_b32_e32 v2, 16, v2
	v_add3_u32 v24, v7, v24, s12
	v_and_or_b32 v24, v24, s11, v2
	v_bfe_u32 v2, v8, 16, 1
	v_add3_u32 v2, v8, v2, s12
	v_bfe_u32 v25, v9, 16, 1
	v_lshrrev_b32_e32 v2, 16, v2
	v_add3_u32 v25, v9, v25, s12
	v_add_co_u32_e32 v26, vcc, s14, v20
	v_and_or_b32 v25, v25, s11, v2
	s_nop 0
	v_addc_co_u32_e32 v27, vcc, 0, v21, vcc
	s_mov_b32 s14, 0xaf19000
	global_store_dwordx2 v[26:27], v[24:25], off sc1
	v_add_co_u32_e32 v24, vcc, s14, v20
	v_mul_f32_e32 v2, 0x3fb8aa3b, v3
	s_nop 0
	v_addc_co_u32_e32 v25, vcc, 0, v21, vcc
	global_load_dwordx2 v[24:25], v[24:25], off
	v_exp_f32_e32 v2, v2
	s_mov_b32 s14, 0x9daa000
	s_waitcnt vmcnt(0)
	v_lshlrev_b32_e32 v26, 16, v24
	v_and_b32_e32 v27, 0xffff0000, v24
	v_lshlrev_b32_e32 v24, 16, v25
	v_and_b32_e32 v25, 0xffff0000, v25
	v_pk_fma_f32 v[8:9], v[8:9], v[2:3], v[24:25] op_sel_hi:[1,0,1]
	v_pk_fma_f32 v[2:3], v[6:7], v[2:3], v[26:27] op_sel_hi:[1,0,1]
	v_bfe_u32 v24, v9, 16, 1
	v_bfe_u32 v6, v2, 16, 1
	v_add3_u32 v6, v2, v6, s12
	v_bfe_u32 v7, v3, 16, 1
	v_lshrrev_b32_e32 v6, 16, v6
	v_add3_u32 v7, v3, v7, s12
	v_and_or_b32 v6, v7, s11, v6
	v_bfe_u32 v7, v8, 16, 1
	v_add3_u32 v7, v8, v7, s12
	v_lshrrev_b32_e32 v7, 16, v7
	v_add3_u32 v24, v9, v24, s12
	v_and_or_b32 v7, v24, s11, v7
	v_add_co_u32_e32 v24, vcc, s14, v20
	s_mov_b32 s14, 0xaf2a000
	s_nop 0
	v_addc_co_u32_e32 v25, vcc, 0, v21, vcc
	global_store_dwordx2 v[24:25], v[6:7], off sc1
	v_add_co_u32_e32 v6, vcc, s14, v20
	s_mov_b32 s14, 0x9dbb000
	s_nop 0
	v_addc_co_u32_e32 v7, vcc, 0, v21, vcc
	global_load_dwordx2 v[6:7], v[6:7], off
	s_waitcnt vmcnt(0)
	v_lshlrev_b32_e32 v24, 16, v6
	v_and_b32_e32 v25, 0xffff0000, v6
	v_lshlrev_b32_e32 v6, 16, v7
	v_and_b32_e32 v7, 0xffff0000, v7
	v_pk_fma_f32 v[2:3], v[2:3], v[4:5], v[24:25] op_sel_hi:[1,0,1]
	v_pk_fma_f32 v[6:7], v[8:9], v[4:5], v[6:7] op_sel_hi:[1,0,1]
	v_bfe_u32 v4, v2, 16, 1
	v_add3_u32 v4, v2, v4, s12
	v_bfe_u32 v8, v3, 16, 1
	v_lshrrev_b32_e32 v4, 16, v4
	v_add3_u32 v8, v3, v8, s12
	v_and_or_b32 v8, v8, s11, v4
	v_bfe_u32 v4, v6, 16, 1
	v_add3_u32 v4, v6, v4, s12
	v_bfe_u32 v9, v7, 16, 1
	v_lshrrev_b32_e32 v4, 16, v4
	v_add3_u32 v9, v7, v9, s12
	v_add_co_u32_e32 v24, vcc, s14, v20
	v_and_or_b32 v9, v9, s11, v4
	s_nop 0
	v_addc_co_u32_e32 v25, vcc, 0, v21, vcc
	s_mov_b32 s14, 0xaf3b000
	global_store_dwordx2 v[24:25], v[8:9], off sc1
	v_add_co_u32_e32 v8, vcc, s14, v20
	v_mul_f32_e32 v4, 0x3fb8aa3b, v5
	s_nop 0
	v_addc_co_u32_e32 v9, vcc, 0, v21, vcc
	global_load_dwordx2 v[8:9], v[8:9], off
	v_exp_f32_e32 v4, v4
	s_mov_b32 s14, 0x9dcc000
	s_waitcnt vmcnt(0)
	v_lshlrev_b32_e32 v24, 16, v8
	v_and_b32_e32 v25, 0xffff0000, v8
	v_lshlrev_b32_e32 v8, 16, v9
	v_and_b32_e32 v9, 0xffff0000, v9
	v_pk_fma_f32 v[2:3], v[2:3], v[4:5], v[24:25] op_sel_hi:[1,0,1]
	v_pk_fma_f32 v[6:7], v[6:7], v[4:5], v[8:9] op_sel_hi:[1,0,1]
	v_bfe_u32 v4, v2, 16, 1
	v_add3_u32 v4, v2, v4, s12
	v_bfe_u32 v5, v3, 16, 1
	v_lshrrev_b32_e32 v4, 16, v4
	v_add3_u32 v5, v3, v5, s12
	v_and_or_b32 v4, v5, s11, v4
	v_bfe_u32 v5, v6, 16, 1
	v_add3_u32 v5, v6, v5, s12
	v_bfe_u32 v8, v7, 16, 1
	v_lshrrev_b32_e32 v5, 16, v5
	v_add3_u32 v8, v7, v8, s12
	v_and_or_b32 v5, v8, s11, v5
	v_add_co_u32_e32 v8, vcc, s14, v20
	s_mov_b32 s14, 0xaf4c000
	s_nop 0
	v_addc_co_u32_e32 v9, vcc, 0, v21, vcc
	global_store_dwordx2 v[8:9], v[4:5], off sc1
	v_add_co_u32_e32 v4, vcc, s14, v20
	s_mov_b32 s14, 0x9ddd000
	s_nop 0
	v_addc_co_u32_e32 v5, vcc, 0, v21, vcc
	global_load_dwordx2 v[4:5], v[4:5], off
	s_waitcnt vmcnt(0)
	v_lshlrev_b32_e32 v8, 16, v4
	v_and_b32_e32 v9, 0xffff0000, v4
	v_lshlrev_b32_e32 v4, 16, v5
	v_and_b32_e32 v5, 0xffff0000, v5
	v_pk_fma_f32 v[2:3], v[2:3], v[10:11], v[8:9] op_sel_hi:[1,0,1]
	v_pk_fma_f32 v[4:5], v[6:7], v[10:11], v[4:5] op_sel_hi:[1,0,1]
	v_bfe_u32 v6, v2, 16, 1
	v_add3_u32 v6, v2, v6, s12
	v_bfe_u32 v7, v3, 16, 1
	v_lshrrev_b32_e32 v6, 16, v6
	v_add3_u32 v7, v3, v7, s12
	v_and_or_b32 v6, v7, s11, v6
	v_bfe_u32 v7, v4, 16, 1
	v_add3_u32 v7, v4, v7, s12
	v_bfe_u32 v8, v5, 16, 1
	v_lshrrev_b32_e32 v7, 16, v7
	v_add3_u32 v8, v5, v8, s12
	v_and_or_b32 v7, v8, s11, v7
	v_add_co_u32_e32 v8, vcc, s14, v20
	s_mov_b32 s14, 0xaf5d000
	s_nop 0
	v_addc_co_u32_e32 v9, vcc, 0, v21, vcc
	global_store_dwordx2 v[8:9], v[6:7], off sc1
	v_add_co_u32_e32 v6, vcc, s14, v20
	v_mul_f32_e32 v10, 0x3fb8aa3b, v11
	s_nop 0
	v_addc_co_u32_e32 v7, vcc, 0, v21, vcc
	global_load_dwordx2 v[6:7], v[6:7], off
	v_exp_f32_e32 v10, v10
	s_mov_b32 s14, 0x9dee000
	s_waitcnt vmcnt(0)
	v_lshlrev_b32_e32 v8, 16, v6
	v_and_b32_e32 v9, 0xffff0000, v6
	v_lshlrev_b32_e32 v6, 16, v7
	v_and_b32_e32 v7, 0xffff0000, v7
	v_pk_fma_f32 v[2:3], v[2:3], v[10:11], v[8:9] op_sel_hi:[1,0,1]
	v_pk_fma_f32 v[4:5], v[4:5], v[10:11], v[6:7] op_sel_hi:[1,0,1]
	v_bfe_u32 v6, v2, 16, 1
	v_add3_u32 v6, v2, v6, s12
	v_bfe_u32 v7, v3, 16, 1
	v_lshrrev_b32_e32 v6, 16, v6
	v_add3_u32 v7, v3, v7, s12
	v_and_or_b32 v6, v7, s11, v6
	v_bfe_u32 v7, v4, 16, 1
	v_add3_u32 v7, v4, v7, s12
	v_bfe_u32 v8, v5, 16, 1
	v_lshrrev_b32_e32 v7, 16, v7
	v_add3_u32 v8, v5, v8, s12
	v_and_or_b32 v7, v8, s11, v7
	v_add_co_u32_e32 v8, vcc, s14, v20
	s_mov_b32 s14, 0xaf6e000
	s_nop 0
	v_addc_co_u32_e32 v9, vcc, 0, v21, vcc
	global_store_dwordx2 v[8:9], v[6:7], off sc1
	v_add_co_u32_e32 v6, vcc, s14, v20
	v_mul_f32_e32 v10, 0x3fb8aa3b, v12
	s_nop 0
	v_addc_co_u32_e32 v7, vcc, 0, v21, vcc
	global_load_dwordx2 v[6:7], v[6:7], off
	v_exp_f32_e32 v10, v10
	s_mov_b64 s[14:15], 0x110000
	v_lshl_add_u64 v[16:17], v[16:17], 0, s[14:15]
	s_waitcnt vmcnt(0)
	v_lshlrev_b32_e32 v8, 16, v6
	v_and_b32_e32 v9, 0xffff0000, v6
	v_lshlrev_b32_e32 v6, 16, v7
	v_and_b32_e32 v7, 0xffff0000, v7
	v_pk_fma_f32 v[2:3], v[2:3], v[10:11], v[8:9] op_sel_hi:[1,0,1]
	v_pk_fma_f32 v[4:5], v[4:5], v[10:11], v[6:7] op_sel_hi:[1,0,1]
	v_bfe_u32 v6, v2, 16, 1
	v_add3_u32 v6, v2, v6, s12
	v_bfe_u32 v7, v3, 16, 1
	v_lshrrev_b32_e32 v6, 16, v6
	v_add3_u32 v7, v3, v7, s12
	v_and_or_b32 v6, v7, s11, v6
	v_bfe_u32 v7, v4, 16, 1
	v_add3_u32 v7, v4, v7, s12
	v_bfe_u32 v8, v5, 16, 1
	v_lshrrev_b32_e32 v7, 16, v7
	v_add3_u32 v8, v5, v8, s12
	v_and_or_b32 v7, v8, s11, v7
	v_add_co_u32_e32 v8, vcc, 0x9dff000, v20
	s_nop 1
	v_addc_co_u32_e32 v9, vcc, 0, v21, vcc
	global_store_dwordx2 v[8:9], v[6:7], off sc1
	s_cbranch_scc0 .LBB0_485
	v_add_u32_e32 v1, s9, v1
	s_mov_b32 s13, 0x10fff
	v_cmp_lt_i32_e32 vcc, s13, v1
	s_or_b64 s[6:7], vcc, s[6:7]
	s_andn2_b64 exec, exec, s[6:7]
	s_cbranch_execnz .LBB0_484

.LBB0_634:
	s_andn2_saveexec_b64 s[44:45], s[56:57]
	s_cbranch_execz .LBB0_654
	s_mov_b64 s[56:57], exec
	s_waitcnt lgkmcnt(0)
	s_waitcnt vmcnt(0)
	v_mbcnt_lo_u32_b32 v7, s56, 0
	v_mbcnt_hi_u32_b32 v7, s57, v7
	v_cmp_eq_u32_e32 vcc, 0, v7
	s_and_saveexec_b64 s[58:59], vcc
	s_cbranch_execz .LBB0_637
	s_bcnt1_i32_b64 s6, s[56:57]
	v_readlane_b32 s44, v255, 5
	v_mov_b32_e32 v9, s6
	v_readlane_b32 s45, v255, 6
	s_nop 4
	global_atomic_add v9, v6, v9, s[44:45] sc0

.LBB0_817:
	v_add_u32_e32 v12, s6, v222
	v_ashrrev_i32_e32 v13, 31, v12
	v_lshlrev_b64 v[12:13], 11, v[12:13]
	v_lshl_add_u64 v[56:57], v[4:5], 0, v[12:13]
	v_add_co_u32_e32 v58, vcc, 0x8000, v56
	global_load_dwordx4 v[12:15], v[56:57], off
	global_load_dwordx4 v[16:19], v[2:3], off
	v_addc_co_u32_e32 v59, vcc, 0, v57, vcc
	v_add_co_u32_e32 v60, vcc, 0x10000, v56
	global_load_dwordx4 v[20:23], v[58:59], off
	s_nop 0
	v_addc_co_u32_e32 v61, vcc, 0, v57, vcc
	v_add_co_u32_e32 v62, vcc, 0x18000, v56
	global_load_dwordx4 v[24:27], v[60:61], off
	s_nop 0
	v_addc_co_u32_e32 v63, vcc, 0, v57, vcc
	global_load_dwordx4 v[28:31], v[62:63], off
	global_load_dwordx4 v[32:35], v[56:57], off offset:64
	global_load_dwordx4 v[36:39], v[2:3], off offset:64
	global_load_dwordx4 v[40:43], v[58:59], off offset:64
	global_load_dwordx4 v[44:47], v[60:61], off offset:64
	global_load_dwordx4 v[48:51], v[62:63], off offset:64
	s_and_b64 vcc, exec, s[4:5]
	s_waitcnt vmcnt(8)
	v_mfma_f32_16x16x32_bf16 v[12:15], v[12:15], v[16:19], 0
	s_waitcnt vmcnt(7)
	v_mfma_f32_16x16x32_bf16 v[20:23], v[20:23], v[16:19], 0
	s_waitcnt vmcnt(6)
	v_mfma_f32_16x16x32_bf16 v[24:27], v[24:27], v[16:19], 0
	s_waitcnt vmcnt(5)
	v_mfma_f32_16x16x32_bf16 v[16:19], v[28:31], v[16:19], 0
	global_load_dwordx4 v[28:31], v[56:57], off offset:128
	global_load_dwordx4 v[52:55], v[2:3], off offset:128
	s_waitcnt vmcnt(5)
	v_mfma_f32_16x16x32_bf16 v[12:15], v[32:35], v[36:39], v[12:15]
	global_load_dwordx4 v[32:35], v[58:59], off offset:128
	s_waitcnt vmcnt(5)
	v_mfma_f32_16x16x32_bf16 v[20:23], v[40:43], v[36:39], v[20:23]
	global_load_dwordx4 v[40:43], v[60:61], off offset:128
	s_waitcnt vmcnt(5)
	v_mfma_f32_16x16x32_bf16 v[24:27], v[44:47], v[36:39], v[24:27]
	global_load_dwordx4 v[44:47], v[62:63], off offset:128
	s_waitcnt vmcnt(5)
	v_mfma_f32_16x16x32_bf16 v[16:19], v[48:51], v[36:39], v[16:19]
	global_load_dwordx4 v[36:39], v[56:57], off offset:192
	global_load_dwordx4 v[48:51], v[2:3], off offset:192
	s_waitcnt vmcnt(5)
	v_mfma_f32_16x16x32_bf16 v[12:15], v[28:31], v[52:55], v[12:15]
	global_load_dwordx4 v[28:31], v[58:59], off offset:192
	s_waitcnt vmcnt(5)
	v_mfma_f32_16x16x32_bf16 v[20:23], v[32:35], v[52:55], v[20:23]
	global_load_dwordx4 v[32:35], v[60:61], off offset:192
	s_waitcnt vmcnt(5)
	v_mfma_f32_16x16x32_bf16 v[24:27], v[40:43], v[52:55], v[24:27]
	global_load_dwordx4 v[40:43], v[62:63], off offset:192
	s_barrier
	s_waitcnt vmcnt(5)
	v_mfma_f32_16x16x32_bf16 v[16:19], v[44:47], v[52:55], v[16:19]
	s_waitcnt vmcnt(3)
	v_mfma_f32_16x16x32_bf16 v[12:15], v[36:39], v[48:51], v[12:15]
	s_waitcnt vmcnt(2)
	v_mfma_f32_16x16x32_bf16 v[20:23], v[28:31], v[48:51], v[20:23]
	s_waitcnt vmcnt(1)
	v_mfma_f32_16x16x32_bf16 v[24:27], v[32:35], v[48:51], v[24:27]
	s_waitcnt vmcnt(0)
	v_mfma_f32_16x16x32_bf16 v[16:19], v[40:43], v[48:51], v[16:19]
	s_nop 1
	ds_write_b128 v11, v[12:15]
	s_nop 0
	ds_write_b128 v11, v[20:23] offset:1024
	s_nop 0
	ds_write_b128 v11, v[24:27] offset:2048
	s_nop 0
	ds_write_b128 v11, v[16:19] offset:3072
	s_waitcnt lgkmcnt(0)
	s_barrier
	s_cbranch_vccnz .LBB0_816
	v_add_u32_e32 v80, s6, v10
	v_ashrrev_i32_e32 v81, 31, v80
	v_lshl_add_u64 v[82:83], v[80:81], 2, v[6:7]
	global_load_dwordx4 v[12:15], v[82:83], off
	ds_read_b128 v[16:19], v1
	ds_read_b128 v[20:23], v1 offset:1024
	ds_read_b128 v[24:27], v1 offset:4096
	ds_read_b128 v[28:31], v1 offset:5120
	ds_read_b128 v[32:35], v1 offset:8192
	ds_read_b128 v[36:39], v1 offset:9216
	ds_read_b128 v[40:43], v1 offset:12288
	ds_read_b128 v[44:47], v1 offset:13312
	ds_read_b128 v[48:51], v1 offset:16384
	ds_read_b128 v[52:55], v1 offset:17408
	ds_read_b128 v[56:59], v1 offset:20480
	ds_read_b128 v[60:63], v1 offset:21504
	ds_read_b128 v[64:67], v1 offset:24576
	ds_read_b128 v[68:71], v1 offset:25600
	ds_read_b128 v[72:75], v1 offset:28672
	ds_read_b128 v[76:79], v1 offset:29696
	s_waitcnt lgkmcnt(13)
	v_pk_add_f32 v[18:19], v[18:19], v[26:27]
	v_pk_add_f32 v[16:17], v[16:17], v[24:25]
	s_waitcnt lgkmcnt(11)
	v_pk_add_f32 v[18:19], v[18:19], v[34:35]
	v_pk_add_f32 v[16:17], v[16:17], v[32:33]
	s_waitcnt lgkmcnt(9)
	v_pk_add_f32 v[18:19], v[18:19], v[42:43]
	v_pk_add_f32 v[16:17], v[16:17], v[40:41]
	s_waitcnt lgkmcnt(7)
	v_pk_add_f32 v[18:19], v[18:19], v[50:51]
	v_pk_add_f32 v[16:17], v[16:17], v[48:49]
	s_waitcnt lgkmcnt(5)
	v_pk_add_f32 v[18:19], v[18:19], v[58:59]
	v_pk_add_f32 v[16:17], v[16:17], v[56:57]
	s_waitcnt lgkmcnt(3)
	v_pk_add_f32 v[18:19], v[18:19], v[66:67]
	v_pk_add_f32 v[16:17], v[16:17], v[64:65]
	s_waitcnt lgkmcnt(1)
	v_pk_add_f32 v[18:19], v[18:19], v[74:75]
	v_pk_add_f32 v[16:17], v[16:17], v[72:73]
	v_lshl_add_u64 v[84:85], v[80:81], 1, v[8:9]
	v_pk_add_f32 v[20:21], v[20:21], v[28:29]
	s_waitcnt vmcnt(0)
	v_pk_add_f32 v[14:15], v[18:19], v[14:15]
	v_pk_add_f32 v[12:13], v[16:17], v[12:13]
	v_bfe_u32 v18, v14, 16, 1
	v_bfe_u32 v16, v12, 16, 1
	v_bfe_u32 v17, v13, 16, 1
	v_bfe_u32 v19, v15, 16, 1
	v_add3_u32 v12, v12, v16, s8
	v_add3_u32 v14, v14, v18, s8
	v_add3_u32 v13, v13, v17, s8
	v_add3_u32 v15, v15, v19, s8
	v_lshrrev_b32_e32 v12, 16, v12
	v_lshrrev_b32_e32 v14, 16, v14
	v_and_or_b32 v12, v13, s9, v12
	v_and_or_b32 v13, v15, s9, v14
	global_store_dwordx2 v[84:85], v[12:13], off sc1
	global_load_dwordx4 v[12:15], v[82:83], off offset:64
	v_pk_add_f32 v[18:19], v[22:23], v[30:31]
	v_pk_add_f32 v[20:21], v[20:21], v[36:37]
	v_pk_add_f32 v[18:19], v[18:19], v[38:39]
	v_pk_add_f32 v[20:21], v[20:21], v[44:45]
	v_pk_add_f32 v[18:19], v[18:19], v[46:47]
	v_pk_add_f32 v[20:21], v[20:21], v[52:53]
	v_pk_add_f32 v[18:19], v[18:19], v[54:55]
	v_pk_add_f32 v[20:21], v[20:21], v[60:61]
	v_pk_add_f32 v[18:19], v[18:19], v[62:63]
	v_pk_add_f32 v[20:21], v[20:21], v[68:69]
	v_pk_add_f32 v[18:19], v[18:19], v[70:71]
	s_waitcnt lgkmcnt(0)
	v_pk_add_f32 v[20:21], v[20:21], v[76:77]
	v_pk_add_f32 v[18:19], v[18:19], v[78:79]
	v_add_u32_e32 v16, 16, v80
	v_ashrrev_i32_e32 v17, 31, v16
	v_lshl_add_u64 v[16:17], v[16:17], 1, v[8:9]
	v_add_u32_e32 v84, 32, v80
	v_ashrrev_i32_e32 v85, 31, v84
	v_lshl_add_u64 v[84:85], v[84:85], 1, v[8:9]
	s_waitcnt vmcnt(0)
	v_pk_add_f32 v[14:15], v[18:19], v[14:15]
	v_pk_add_f32 v[12:13], v[20:21], v[12:13]
	v_bfe_u32 v20, v14, 16, 1
	v_bfe_u32 v18, v12, 16, 1
	v_bfe_u32 v19, v13, 16, 1
	v_bfe_u32 v21, v15, 16, 1
	v_add3_u32 v12, v12, v18, s8
	v_add3_u32 v14, v14, v20, s8
	v_add3_u32 v13, v13, v19, s8
	v_add3_u32 v15, v15, v21, s8
	v_lshrrev_b32_e32 v12, 16, v12
	v_lshrrev_b32_e32 v14, 16, v14
	v_and_or_b32 v12, v13, s9, v12
	v_and_or_b32 v13, v15, s9, v14
	global_store_dwordx2 v[16:17], v[12:13], off sc1
	global_load_dwordx4 v[12:15], v[82:83], off offset:128
	ds_read_b128 v[16:19], v1 offset:2048
	ds_read_b128 v[20:23], v1 offset:3072
	ds_read_b128 v[24:27], v1 offset:6144
	ds_read_b128 v[28:31], v1 offset:7168
	ds_read_b128 v[32:35], v1 offset:10240
	ds_read_b128 v[36:39], v1 offset:11264
	ds_read_b128 v[40:43], v1 offset:14336
	ds_read_b128 v[44:47], v1 offset:15360
	ds_read_b128 v[48:51], v1 offset:18432
	ds_read_b128 v[52:55], v1 offset:19456
	ds_read_b128 v[56:59], v1 offset:22528
	ds_read_b128 v[60:63], v1 offset:23552
	ds_read_b128 v[64:67], v1 offset:26624
	ds_read_b128 v[68:71], v1 offset:27648
	ds_read_b128 v[72:75], v1 offset:30720
	ds_read_b128 v[76:79], v1 offset:31744
	s_waitcnt lgkmcnt(13)
	v_pk_add_f32 v[18:19], v[18:19], v[26:27]
	v_pk_add_f32 v[16:17], v[16:17], v[24:25]
	s_waitcnt lgkmcnt(11)
	v_pk_add_f32 v[18:19], v[18:19], v[34:35]
	v_pk_add_f32 v[16:17], v[16:17], v[32:33]
	s_waitcnt lgkmcnt(9)
	v_pk_add_f32 v[18:19], v[18:19], v[42:43]
	v_pk_add_f32 v[16:17], v[16:17], v[40:41]
	s_waitcnt lgkmcnt(7)
	v_pk_add_f32 v[18:19], v[18:19], v[50:51]
	v_pk_add_f32 v[16:17], v[16:17], v[48:49]
	s_waitcnt lgkmcnt(5)
	v_pk_add_f32 v[18:19], v[18:19], v[58:59]
	v_pk_add_f32 v[16:17], v[16:17], v[56:57]
	s_waitcnt lgkmcnt(3)
	v_pk_add_f32 v[18:19], v[18:19], v[66:67]
	v_pk_add_f32 v[16:17], v[16:17], v[64:65]
	s_waitcnt lgkmcnt(1)
	v_pk_add_f32 v[18:19], v[18:19], v[74:75]
	v_pk_add_f32 v[16:17], v[16:17], v[72:73]
	v_pk_add_f32 v[20:21], v[20:21], v[28:29]
	s_waitcnt vmcnt(0)
	v_pk_add_f32 v[14:15], v[18:19], v[14:15]
	v_pk_add_f32 v[12:13], v[16:17], v[12:13]
	v_bfe_u32 v18, v14, 16, 1
	v_bfe_u32 v16, v12, 16, 1
	v_bfe_u32 v17, v13, 16, 1
	v_bfe_u32 v19, v15, 16, 1
	v_add3_u32 v12, v12, v16, s8
	v_add3_u32 v14, v14, v18, s8
	v_add3_u32 v13, v13, v17, s8
	v_add3_u32 v15, v15, v19, s8
	v_lshrrev_b32_e32 v12, 16, v12
	v_lshrrev_b32_e32 v14, 16, v14
	v_and_or_b32 v12, v13, s9, v12
	v_and_or_b32 v13, v15, s9, v14
	global_store_dwordx2 v[84:85], v[12:13], off sc1
	global_load_dwordx4 v[12:15], v[82:83], off offset:192
	v_pk_add_f32 v[18:19], v[22:23], v[30:31]
	v_pk_add_f32 v[20:21], v[20:21], v[36:37]
	v_pk_add_f32 v[18:19], v[18:19], v[38:39]
	v_pk_add_f32 v[20:21], v[20:21], v[44:45]
	v_pk_add_f32 v[18:19], v[18:19], v[46:47]
	v_pk_add_f32 v[20:21], v[20:21], v[52:53]
	v_pk_add_f32 v[18:19], v[18:19], v[54:55]
	v_pk_add_f32 v[20:21], v[20:21], v[60:61]
	v_pk_add_f32 v[18:19], v[18:19], v[62:63]
	v_pk_add_f32 v[20:21], v[20:21], v[68:69]
	v_pk_add_f32 v[18:19], v[18:19], v[70:71]
	s_waitcnt lgkmcnt(0)
	v_pk_add_f32 v[20:21], v[20:21], v[76:77]
	v_pk_add_f32 v[18:19], v[18:19], v[78:79]
	v_add_u32_e32 v16, 48, v80
	v_ashrrev_i32_e32 v17, 31, v16
	s_waitcnt vmcnt(0)
	v_pk_add_f32 v[14:15], v[18:19], v[14:15]
	v_pk_add_f32 v[12:13], v[20:21], v[12:13]
	v_bfe_u32 v20, v14, 16, 1
	v_bfe_u32 v18, v12, 16, 1
	v_bfe_u32 v19, v13, 16, 1
	v_bfe_u32 v21, v15, 16, 1
	v_add3_u32 v12, v12, v18, s8
	v_add3_u32 v14, v14, v20, s8
	v_add3_u32 v13, v13, v19, s8
	v_add3_u32 v15, v15, v21, s8
	v_lshrrev_b32_e32 v12, 16, v12
	v_lshrrev_b32_e32 v14, 16, v14
	v_and_or_b32 v12, v13, s9, v12
	v_and_or_b32 v13, v15, s9, v14
	v_lshl_add_u64 v[14:15], v[16:17], 1, v[8:9]
	global_store_dwordx2 v[14:15], v[12:13], off sc1
	s_branch .LBB0_816

.LBB0_940:
	s_or_b64 exec, exec, s[8:9]
	s_waitcnt lgkmcnt(0)
	s_barrier
	s_and_saveexec_b64 s[6:7], s[4:5]
	s_cbranch_execz .LBB0_943
	v_lshl_add_u32 v1, v0, 2, 0
	v_add_u32_e32 v1, 0x1ee80, v1
	ds_read_b32 v1, v1
	s_waitcnt lgkmcnt(0)
	v_cmp_lt_i32_e32 vcc, -1, v1
	s_and_b64 exec, exec, vcc
	s_cbranch_execz .LBB0_943
	v_bfe_u32 v2, v1, 8, 8
	v_mul_u32_u24_e32 v6, 0x4010, v2
	v_lshl_add_u32 v2, v2, 2, 0
	v_add_u32_e32 v2, 0x1ee00, v2
	ds_read_b32 v7, v2
	v_lshl_add_u32 v2, v0, 4, 0
	v_add_u32_e32 v2, 0x1f180, v2
	ds_read_b128 v[2:5], v2
	v_and_b32_e32 v8, 0xff, v1
	s_waitcnt lgkmcnt(1)
	v_add3_u32 v6, v6, v8, v7
	v_ashrrev_i32_e32 v7, 31, v6
	v_lshrrev_b32_e32 v1, 16, v1
	v_lshl_add_u64 v[8:9], v[6:7], 2, s[24:25]
	v_lshl_add_u64 v[6:7], v[6:7], 4, s[28:29]
	global_store_dword v[8:9], v1, off sc1
	s_waitcnt lgkmcnt(0)
	global_store_dwordx4 v[6:7], v[2:5], off sc1

.LBB0_1217:
	s_or_b64 exec, exec, s[8:9]
	ds_read_b128 v[52:55], v42
	ds_read_b128 v[56:59], v42 offset:64
	ds_read_b128 v[60:63], v42 offset:32768
	ds_read_b128 v[64:67], v42 offset:32832
	s_lshl_b32 s8, s37, 9
	s_and_b32 s8, s8, 0x200
	s_waitcnt lgkmcnt(3)
	v_mfma_f32_16x16x32_bf16 v[52:55], v[30:33], v[52:55], 0
	s_lshl_b32 s9, s8, 4
	s_add_i32 s9, s9, 0
	s_add_i32 s9, s9, 0x10400
	s_waitcnt lgkmcnt(1)
	v_mfma_f32_16x16x32_bf16 v[30:33], v[30:33], v[60:63], v[52:55]
	s_add_i32 s14, s9, s19
	v_mfma_f32_16x16x32_bf16 v[30:33], v[26:29], v[56:59], v[30:33]
	s_waitcnt lgkmcnt(0)
	v_mfma_f32_16x16x32_bf16 v[26:29], v[26:29], v[64:67], v[30:33]
	s_nop 5
	ds_read_b128 v[30:33], v42 offset:128
	ds_read_b128 v[52:55], v42 offset:192
	s_waitcnt lgkmcnt(1)
	v_mfma_f32_16x16x32_bf16 v[26:29], v[22:25], v[30:33], v[26:29]
	ds_read_b128 v[30:33], v42 offset:32896
	ds_read_b128 v[56:59], v42 offset:32960
	s_waitcnt lgkmcnt(1)
	v_mfma_f32_16x16x32_bf16 v[22:25], v[22:25], v[30:33], v[26:29]
	v_mfma_f32_16x16x32_bf16 v[22:25], v[18:21], v[52:55], v[22:25]
	s_waitcnt lgkmcnt(0)
	v_mfma_f32_16x16x32_bf16 v[18:21], v[18:21], v[56:59], v[22:25]
	s_nop 5
	v_lshl_add_u32 v22, v208, 4, s14
	s_nop 0
	ds_write_b128 v22, v[18:21]
	s_waitcnt lgkmcnt(0)
	s_barrier
	s_and_saveexec_b64 s[14:15], s[4:5]
	s_cbranch_execz .LBB0_1212
	v_lshlrev_b32_e32 v18, 2, v44
	v_add3_u32 v26, s9, v47, v18
	v_add_u32_e32 v27, s8, v46
	ds_read2st64_b32 v[18:19], v26 offset1:4
	ds_read2_b32 v[20:21], v27 offset1:16
	ds_read2st64_b32 v[22:23], v26 offset0:8 offset1:12
	ds_read2_b32 v[24:25], v27 offset0:32 offset1:48
	s_lshl_b32 s9, s37, 4
	s_add_i32 s38, s9, s16
	s_waitcnt lgkmcnt(3)
	v_add_f32_e32 v18, 0, v18
	s_waitcnt lgkmcnt(2)
	v_add_f32_e32 v20, 0, v20
	v_add_f32_e32 v18, v18, v19
	v_add_f32_e32 v19, v20, v21
	s_waitcnt lgkmcnt(1)
	v_add_f32_e32 v22, v18, v22
	s_waitcnt lgkmcnt(0)
	v_add_f32_e32 v24, v19, v24
	ds_read2st64_b32 v[18:19], v26 offset0:16 offset1:20
	ds_read2_b32 v[20:21], v27 offset0:64 offset1:80
	v_add_f32_e32 v28, v22, v23
	ds_read2_b32 v[22:23], v27 offset0:96 offset1:112
	v_add_f32_e32 v24, v24, v25
	s_waitcnt lgkmcnt(2)
	v_add_f32_e32 v18, v28, v18
	s_waitcnt lgkmcnt(1)
	v_add_f32_e32 v20, v24, v20
	v_add_f32_e32 v24, v20, v21
	s_waitcnt lgkmcnt(0)
	v_add_f32_e32 v22, v24, v22
	v_add_f32_e32 v22, v22, v23
	v_fmamk_f32 v22, v22, 0x3a800000, v48
	v_mul_f32_e32 v23, 0x4b800000, v22
	v_cmp_gt_f32_e64 s[8:9], s20, v22
	ds_read2st64_b32 v[20:21], v26 offset0:24 offset1:28
	v_add_f32_e32 v18, v18, v19
	v_cndmask_b32_e64 v22, v22, v23, s[8:9]
	v_rsq_f32_e32 v22, v22
	s_cmp_lt_u32 s37, 4
	s_waitcnt lgkmcnt(0)
	v_add_f32_e32 v18, v18, v20
	v_add_f32_e32 v18, v18, v21
	v_mul_f32_e32 v19, 0x45800000, v22
	v_cndmask_b32_e64 v20, v22, v19, s[8:9]
	v_fma_f32 v18, v18, v20, v1
	v_mul_f32_e64 v19, |v18|, s21
	v_fma_f32 v21, |v18|, s21, -v19
	v_rndne_f32_e32 v22, v19
	v_fma_f32 v21, |v18|, s22, v21
	v_sub_f32_e32 v19, v19, v22
	v_add_f32_e32 v19, v19, v21
	v_exp_f32_e32 v19, v19
	v_cvt_i32_f32_e32 v21, v22
	v_cmp_ngt_f32_e64 s[8:9], |v18|, s23
	v_min_f32_e32 v51, 0, v18
	s_cselect_b32 s37, s38, 0x4000
	v_ldexp_f32 v19, v19, v21
	v_cndmask_b32_e64 v19, 0, v19, s[8:9]
	v_cmp_nlt_f32_e64 s[8:9], |v18|, s30
	s_nop 1
	v_cndmask_b32_e64 v21, v50, v19, s[8:9]
	v_add_f32_e32 v22, 1.0, v21
	v_add_f32_e32 v18, -1.0, v22
	v_sub_f32_e32 v19, v18, v22
	v_add_f32_e32 v19, 1.0, v19
	v_sub_f32_e32 v18, v21, v18
	v_add_f32_e32 v23, v18, v19
	v_frexp_mant_f32_e32 v24, v22
	v_cvt_f64_f32_e32 v[18:19], v22
	v_frexp_exp_i32_f64_e32 v18, v[18:19]
	v_cmp_gt_f32_e64 s[8:9], s34, v24
	s_nop 1
	v_subbrev_co_u32_e64 v28, s[8:9], 0, v18, s[8:9]
	v_sub_u32_e32 v18, 0, v28
	v_ldexp_f32 v19, v22, v18
	v_add_f32_e32 v22, -1.0, v19
	v_add_f32_e32 v24, 1.0, v19
	v_ldexp_f32 v18, v23, v18
	v_add_f32_e32 v23, 1.0, v22
	v_add_f32_e32 v25, -1.0, v24
	v_sub_f32_e32 v23, v19, v23
	v_sub_f32_e32 v19, v19, v25
	v_add_f32_e32 v23, v18, v23
	v_add_f32_e32 v18, v18, v19
	v_add_f32_e32 v29, v24, v18
	v_rcp_f32_e32 v31, v29
	v_sub_f32_e32 v19, v24, v29
	v_add_f32_e32 v30, v18, v19
	v_add_f32_e32 v19, v22, v23
	v_mul_f32_e32 v33, v19, v31
	v_sub_f32_e32 v18, v22, v19
	v_mul_f32_e32 v22, v29, v33
	v_fma_f32 v24, v33, v29, -v22
	v_fmac_f32_e32 v24, v33, v30
	v_add_f32_e32 v32, v23, v18
	v_add_f32_e32 v18, v22, v24
	v_sub_f32_e32 v23, v19, v18
	v_pk_add_f32 v[26:27], v[18:19], v[22:23] neg_lo:[0,1] neg_hi:[0,1]
	v_mov_b32_e32 v25, v18
	v_pk_add_f32 v[18:19], v[26:27], v[24:25] neg_lo:[0,1] neg_hi:[0,1]
	v_cmp_neq_f32_e64 s[8:9], s31, v21
	v_add_f32_e32 v19, v32, v19
	v_add_f32_e32 v18, v18, v19
	v_add_f32_e32 v19, v23, v18
	v_mul_f32_e32 v32, v31, v19
	v_mul_f32_e32 v22, v29, v32
	v_fma_f32 v24, v32, v29, -v22
	v_fmac_f32_e32 v24, v32, v30
	v_sub_f32_e32 v23, v23, v19
	v_add_f32_e32 v29, v18, v23
	v_add_f32_e32 v18, v22, v24
	v_sub_f32_e32 v23, v19, v18
	v_pk_add_f32 v[26:27], v[18:19], v[22:23] neg_lo:[0,1] neg_hi:[0,1]
	v_mov_b32_e32 v25, v18
	v_pk_add_f32 v[18:19], v[26:27], v[24:25] neg_lo:[0,1] neg_hi:[0,1]
	s_nop 0
	v_add_f32_e32 v19, v29, v19
	v_add_f32_e32 v18, v18, v19
	v_add_f32_e32 v19, v33, v32
	v_add_f32_e32 v18, v23, v18
	v_sub_f32_e32 v22, v19, v33
	v_mul_f32_e32 v18, v31, v18
	v_sub_f32_e32 v22, v32, v22
	v_add_f32_e32 v22, v22, v18
	v_add_f32_e32 v24, v19, v22
	v_mul_f32_e32 v25, v24, v24
	v_fmamk_f32 v18, v25, 0x3e9b6dac, v49
	v_fmaak_f32 v39, v25, v18, 0x3f2aaada
	v_cvt_f32_i32_e32 v18, v28
	v_sub_f32_e32 v19, v24, v19
	v_sub_f32_e32 v19, v22, v19
	v_ldexp_f32 v26, v19, 1
	v_mul_f32_e32 v19, v24, v25
	v_ldexp_f32 v23, v24, 1
	v_pk_mul_f32 v[24:25], v[18:19], v[38:39]
	s_nop 0
	v_fma_f32 v22, v18, s35, -v24
	v_fmac_f32_e32 v22, 0xb102e308, v18
	v_pk_add_f32 v[18:19], v[24:25], v[22:23]
	s_nop 0
	v_sub_f32_e32 v23, v19, v23
	v_sub_f32_e32 v23, v25, v23
	v_add_f32_e32 v27, v26, v23
	v_mov_b32_e32 v26, v24
	v_pk_add_f32 v[24:25], v[18:19], v[24:25] neg_lo:[0,1] neg_hi:[0,1]
	v_pk_add_f32 v[28:29], v[18:19], v[26:27]
	v_mov_b32_e32 v23, v18
	v_mov_b32_e32 v25, v29
	v_pk_add_f32 v[30:31], v[22:23], v[24:25] neg_lo:[0,1] neg_hi:[0,1]
	v_pk_add_f32 v[22:23], v[22:23], v[24:25]
	v_mov_b32_e32 v26, v27
	v_pk_add_f32 v[24:25], v[22:23], v[18:19] op_sel:[1,0] op_sel_hi:[0,1] neg_lo:[0,1] neg_hi:[0,1]
	v_pk_add_f32 v[32:33], v[28:29], v[24:25] op_sel_hi:[1,0] neg_lo:[0,1] neg_hi:[0,1]
	v_mov_b32_e32 v28, v29
	v_mov_b32_e32 v29, v23
	v_pk_mov_b32 v[24:25], v[18:19], v[24:25] op_sel:[1,0]
	v_mov_b32_e32 v27, v18
	v_pk_add_f32 v[24:25], v[28:29], v[24:25] neg_lo:[0,1] neg_hi:[0,1]
	v_mov_b32_e32 v32, v30
	v_pk_add_f32 v[18:19], v[26:27], v[24:25] neg_lo:[0,1] neg_hi:[0,1]
	v_mov_b32_e32 v31, v23
	v_pk_add_f32 v[24:25], v[32:33], v[18:19]
	s_nop 0
	v_pk_add_f32 v[26:27], v[24:25], v[24:25] op_sel:[0,1] op_sel_hi:[1,0]
	s_nop 0
	v_pk_add_f32 v[22:23], v[22:23], v[26:27] op_sel:[1,0] op_sel_hi:[0,1]
	v_mov_b32_e32 v25, v22
	v_pk_add_f32 v[28:29], v[24:25], v[30:31] neg_lo:[0,1] neg_hi:[0,1]
	v_mov_b32_e32 v19, v26
	v_sub_f32_e32 v23, v24, v28
	v_pk_add_f32 v[18:19], v[18:19], v[28:29] neg_lo:[0,1] neg_hi:[0,1]
	v_sub_f32_e32 v23, v30, v23
	v_add_f32_e32 v18, v18, v23
	v_add_f32_e32 v18, v18, v19
	v_add_f32_e32 v18, v22, v18
	v_cndmask_b32_e64 v18, v50, v18, s[8:9]
	v_cmp_lt_f32_e64 s[8:9], |v21|, s36
	s_nop 1
	v_cndmask_b32_e64 v18, v18, v21, s[8:9]
	v_sub_f32_e32 v21, v51, v18
	v_or_b32_e32 v18, s37, v45
	v_ashrrev_i32_e32 v19, 31, v18
	v_lshl_add_u64 v[22:23], v[18:19], 2, v[36:37]
	global_store_dword v[22:23], v21, off sc1
	s_and_b64 exec, exec, s[6:7]
	s_cbranch_execz .LBB0_1212
	v_lshl_add_u64 v[18:19], v[18:19], 2, s[0:1]
	global_store_dword v[18:19], v20, off sc1
	s_branch .LBB0_1212

.LBB0_1253:
	s_andn2_saveexec_b64 s[8:9], s[8:9]
	s_cbranch_execz .LBB0_1273
	s_mov_b64 s[8:9], exec
	s_waitcnt lgkmcnt(0)
	s_waitcnt vmcnt(0)
	v_mbcnt_lo_u32_b32 v2, s8, 0
	v_mbcnt_hi_u32_b32 v2, s9, v2
	v_cmp_eq_u32_e32 vcc, 0, v2
	s_and_saveexec_b64 s[12:13], vcc
	s_cbranch_execz .LBB0_1256
	s_bcnt1_i32_b64 s8, s[8:9]
	v_mov_b32_e32 v3, 0x7000
	v_mov_b32_e32 v4, s8
	global_atomic_add v3, v3, v4, s[54:55] offset:1024 sc0

.LBB0_1334:
	s_waitcnt lgkmcnt(0)
	v_add_f32_e32 v22, v23, v22
	v_add_f32_e32 v22, v22, v25
	v_add_f32_e32 v22, v22, v24
	v_add_f32_e32 v22, v22, v27
	v_add_f32_e32 v22, v22, v26
	v_add_f32_e32 v22, v22, v29
	v_cmp_gt_u32_e64 s[8:9], 32, v208
	s_nop 1
	v_cndmask_b32_e64 v20, v21, v20, s[8:9]
	v_add_f32_e32 v21, v22, v28
	s_mul_i32 s8, s18, 0x8100
	v_add_f32_e32 v20, v20, v21
	s_mul_hi_i32 s9, s18, 0x8100
	s_add_u32 s8, s54, s8
	v_sub_f32_e32 v19, v20, v19
	s_addc_u32 s9, s55, s9
	s_and_saveexec_b64 s[10:11], vcc
	s_cbranch_execz .LBB0_1350
	v_add_u32_e32 v20, 48, v1
	v_cndmask_b32_e64 v20, v20, 0, s[78:79]
	v_lshlrev_b32_e32 v20, 2, v20
	v_add_f32_e32 v19, v9, v19
	v_add_u32_e32 v21, 0, v20
	v_mul_f32_e32 v9, 0x3fb8aa3b, v19
	global_store_dword v20, v9, s[8:9] sc1
	ds_write_b32 v21, v9 offset:1024
	s_or_b64 exec, exec, s[10:11]
	s_and_saveexec_b64 s[10:11], vcc
	s_cbranch_execnz .LBB0_1351

.LBB0_1337:
	v_add_u32_e32 v2, 50, v1
	v_cndmask_b32_e64 v2, v2, 2, s[78:79]
	v_lshlrev_b32_e32 v2, 2, v2
	v_add_f32_e32 v19, v10, v19
	v_add_u32_e32 v9, 0, v2
	v_mul_f32_e32 v10, 0x3fb8aa3b, v19
	global_store_dword v2, v10, s[8:9] sc1
	ds_write_b32 v9, v10 offset:1024
	s_or_b64 exec, exec, s[10:11]
	s_and_saveexec_b64 s[10:11], vcc
	s_cbranch_execnz .LBB0_1353

.LBB0_1339:
	v_add_u32_e32 v2, 52, v1
	v_cndmask_b32_e64 v2, v2, 4, s[78:79]
	v_lshlrev_b32_e32 v2, 2, v2
	v_add_f32_e32 v19, v11, v19
	v_add_u32_e32 v3, 0, v2
	v_mul_f32_e32 v9, 0x3fb8aa3b, v19
	global_store_dword v2, v9, s[8:9] sc1
	ds_write_b32 v3, v9 offset:1024
	s_or_b64 exec, exec, s[10:11]
	s_and_saveexec_b64 s[10:11], vcc
	s_cbranch_execnz .LBB0_1355

.LBB0_1341:
	v_add_u32_e32 v2, 54, v1
	v_cndmask_b32_e64 v2, v2, 6, s[78:79]
	v_lshlrev_b32_e32 v2, 2, v2
	v_add_f32_e32 v19, v12, v19
	v_add_u32_e32 v3, 0, v2
	v_mul_f32_e32 v4, 0x3fb8aa3b, v19
	global_store_dword v2, v4, s[8:9] sc1
	ds_write_b32 v3, v4 offset:1024
	s_or_b64 exec, exec, s[10:11]
	s_and_saveexec_b64 s[10:11], vcc
	s_cbranch_execnz .LBB0_1357

.LBB0_1343:
	v_add_u32_e32 v2, 56, v1
	v_cndmask_b32_e64 v2, v2, 8, s[78:79]
	v_lshlrev_b32_e32 v2, 2, v2
	v_add_f32_e32 v19, v13, v19
	v_add_u32_e32 v3, 0, v2
	v_mul_f32_e32 v4, 0x3fb8aa3b, v19
	global_store_dword v2, v4, s[8:9] sc1
	ds_write_b32 v3, v4 offset:1024
	s_or_b64 exec, exec, s[10:11]
	s_and_saveexec_b64 s[10:11], vcc
	s_cbranch_execnz .LBB0_1359

.LBB0_1345:
	v_add_u32_e32 v2, 58, v1
	v_cndmask_b32_e64 v2, v2, 10, s[78:79]
	v_lshlrev_b32_e32 v2, 2, v2
	v_add_f32_e32 v19, v14, v19
	v_add_u32_e32 v3, 0, v2
	v_mul_f32_e32 v4, 0x3fb8aa3b, v19
	global_store_dword v2, v4, s[8:9] sc1
	ds_write_b32 v3, v4 offset:1024
	s_or_b64 exec, exec, s[10:11]
	s_and_saveexec_b64 s[10:11], vcc
	s_cbranch_execnz .LBB0_1361

.LBB0_1347:
	v_add_u32_e32 v2, 60, v1
	v_cndmask_b32_e64 v2, v2, 12, s[78:79]
	v_lshlrev_b32_e32 v2, 2, v2
	v_add_f32_e32 v19, v16, v19
	v_add_u32_e32 v3, 0, v2
	v_mul_f32_e32 v4, 0x3fb8aa3b, v19
	global_store_dword v2, v4, s[8:9] sc1
	ds_write_b32 v3, v4 offset:1024
	s_or_b64 exec, exec, s[10:11]
	s_and_saveexec_b64 s[10:11], vcc
	s_cbranch_execnz .LBB0_1363

.LBB0_1349:
	v_add_u32_e32 v2, 62, v1
	v_cndmask_b32_e64 v2, v2, 14, s[78:79]
	v_add_f32_e32 v4, v17, v19
	v_lshlrev_b32_e32 v2, 2, v2
	v_mul_f32_e32 v5, 0x3fb8aa3b, v4
	v_add_u32_e32 v3, 0, v2
	global_store_dword v2, v5, s[8:9] sc1
	v_add_u32_e32 v2, 63, v1
	v_cndmask_b32_e64 v2, v2, 15, s[78:79]
	v_add_f32_e32 v4, v15, v4
	ds_write_b32 v3, v5 offset:1024
	v_lshlrev_b32_e32 v2, 2, v2
	v_mul_f32_e32 v5, 0x3fb8aa3b, v4
	v_add_u32_e32 v3, 0, v2
	global_store_dword v2, v5, s[8:9] sc1
	v_add_f32_e32 v2, v18, v4
	v_lshlrev_b32_e32 v1, 2, v1
	ds_write_b32 v3, v5 offset:1024
	v_mul_f32_e32 v2, 0x3fb8aa3b, v2
	v_add_u32_e32 v3, 0, v1
	global_store_dword v1, v2, s[8:9] offset:256 sc1
	ds_write_b32 v3, v2 offset:1280
	s_or_b64 exec, exec, s[10:11]
	v_cmp_gt_u32_e32 vcc, 48, v0
	s_and_saveexec_b64 s[4:5], vcc
	s_cbranch_execnz .LBB0_1365
	s_branch .LBB0_1366

.LBB0_1351:
	v_add_u32_e32 v9, 49, v1
	v_cndmask_b32_e64 v9, v9, 1, s[78:79]
	v_lshlrev_b32_e32 v9, 2, v9
	v_add_f32_e32 v19, v2, v19
	v_add_u32_e32 v20, 0, v9
	v_mul_f32_e32 v2, 0x3fb8aa3b, v19
	global_store_dword v9, v2, s[8:9] sc1
	ds_write_b32 v20, v2 offset:1024
	s_or_b64 exec, exec, s[10:11]
	s_and_saveexec_b64 s[10:11], vcc
	s_cbranch_execnz .LBB0_1337

.LBB0_1353:
	v_add_u32_e32 v2, 51, v1
	v_cndmask_b32_e64 v2, v2, 3, s[78:79]
	v_lshlrev_b32_e32 v2, 2, v2
	v_add_f32_e32 v19, v3, v19
	v_add_u32_e32 v9, 0, v2
	v_mul_f32_e32 v3, 0x3fb8aa3b, v19
	global_store_dword v2, v3, s[8:9] sc1
	ds_write_b32 v9, v3 offset:1024
	s_or_b64 exec, exec, s[10:11]
	s_and_saveexec_b64 s[10:11], vcc
	s_cbranch_execnz .LBB0_1339

.LBB0_1355:
	v_add_u32_e32 v2, 53, v1
	v_cndmask_b32_e64 v2, v2, 5, s[78:79]
	v_lshlrev_b32_e32 v2, 2, v2
	v_add_f32_e32 v19, v4, v19
	v_add_u32_e32 v3, 0, v2
	v_mul_f32_e32 v4, 0x3fb8aa3b, v19
	global_store_dword v2, v4, s[8:9] sc1
	ds_write_b32 v3, v4 offset:1024
	s_or_b64 exec, exec, s[10:11]
	s_and_saveexec_b64 s[10:11], vcc
	s_cbranch_execnz .LBB0_1341

.LBB0_1357:
	v_add_u32_e32 v2, 55, v1
	v_cndmask_b32_e64 v2, v2, 7, s[78:79]
	v_lshlrev_b32_e32 v2, 2, v2
	v_add_f32_e32 v19, v5, v19
	v_add_u32_e32 v3, 0, v2
	v_mul_f32_e32 v4, 0x3fb8aa3b, v19
	global_store_dword v2, v4, s[8:9] sc1
	ds_write_b32 v3, v4 offset:1024
	s_or_b64 exec, exec, s[10:11]
	s_and_saveexec_b64 s[10:11], vcc
	s_cbranch_execnz .LBB0_1343

.LBB0_1359:
	v_add_u32_e32 v2, 57, v1
	v_cndmask_b32_e64 v2, v2, 9, s[78:79]
	v_lshlrev_b32_e32 v2, 2, v2
	v_add_f32_e32 v19, v6, v19
	v_add_u32_e32 v3, 0, v2
	v_mul_f32_e32 v4, 0x3fb8aa3b, v19
	global_store_dword v2, v4, s[8:9] sc1
	ds_write_b32 v3, v4 offset:1024
	s_or_b64 exec, exec, s[10:11]
	s_and_saveexec_b64 s[10:11], vcc
	s_cbranch_execnz .LBB0_1345

.LBB0_1361:
	v_add_u32_e32 v2, 59, v1
	v_cndmask_b32_e64 v2, v2, 11, s[78:79]
	v_lshlrev_b32_e32 v2, 2, v2
	v_add_f32_e32 v19, v7, v19
	v_add_u32_e32 v3, 0, v2
	v_mul_f32_e32 v4, 0x3fb8aa3b, v19
	global_store_dword v2, v4, s[8:9] sc1
	ds_write_b32 v3, v4 offset:1024
	s_or_b64 exec, exec, s[10:11]
	s_and_saveexec_b64 s[10:11], vcc
	s_cbranch_execnz .LBB0_1347

.LBB0_1363:
	v_add_u32_e32 v2, 61, v1
	v_cndmask_b32_e64 v2, v2, 13, s[78:79]
	v_lshlrev_b32_e32 v2, 2, v2
	v_add_f32_e32 v19, v8, v19
	v_add_u32_e32 v3, 0, v2
	v_mul_f32_e32 v4, 0x3fb8aa3b, v19
	global_store_dword v2, v4, s[8:9] sc1
	ds_write_b32 v3, v4 offset:1024
	s_or_b64 exec, exec, s[10:11]
	s_and_saveexec_b64 s[10:11], s[4:5]
	s_cbranch_execnz .LBB0_1349

.LBB0_1365:
	v_lshlrev_b32_e32 v1, 2, v0
	v_add_u32_e32 v2, 0, v1
	v_mov_b32_e32 v3, 0x7f800000
	global_store_dword v1, v3, s[8:9] offset:64 sc1
	ds_write_b32 v2, v3 offset:1088

.LBB0_1371:
	s_or_b64 exec, exec, s[4:5]
	s_waitcnt lgkmcnt(0)
	s_barrier
	s_and_saveexec_b64 s[4:5], s[6:7]
	s_cbranch_execz .LBB0_1373
	v_lshl_add_u32 v1, v0, 2, 0
	ds_read_b32 v1, v1 offset:128
	v_lshl_or_b32 v2, s18, 5, v0
	v_readlane_b32 s36, v253, 46
	v_ashrrev_i32_e32 v3, 31, v2
	v_readlane_b32 s50, v253, 60
	v_readlane_b32 s51, v253, 61
	s_waitcnt lgkmcnt(0)
	v_min_i32_e32 v1, v1, v252
	v_and_b32_e32 v1, -2, v1
	v_lshl_add_u64 v[2:3], v[2:3], 2, s[50:51]
	v_add_co_u32_e32 v2, vcc, 0x1582000, v2
	v_readlane_b32 s37, v253, 47
	s_nop 0
	v_addc_co_u32_e32 v3, vcc, 0, v3, vcc
	v_readlane_b32 s38, v253, 48
	v_readlane_b32 s39, v253, 49
	v_readlane_b32 s40, v253, 50
	v_readlane_b32 s41, v253, 51
	v_readlane_b32 s42, v253, 52
	v_readlane_b32 s43, v253, 53
	v_readlane_b32 s44, v253, 54
	v_readlane_b32 s45, v253, 55
	v_readlane_b32 s46, v253, 56
	v_readlane_b32 s47, v253, 57
	v_readlane_b32 s48, v253, 58
	v_readlane_b32 s49, v253, 59
	global_store_dword v[2:3], v1, off sc1

.LBB0_1447:
	v_bfe_u32 v13, v14, 16, 1
	v_add3_u32 v13, v14, v13, s17
	v_bfe_u32 v14, v15, 16, 1
	v_lshrrev_b32_e32 v13, 16, v13
	v_add3_u32 v14, v15, v14, s17
	v_and_or_b32 v14, v14, s18, v13
	v_bfe_u32 v13, v18, 16, 1
	v_add3_u32 v13, v18, v13, s17
	v_bfe_u32 v15, v19, 16, 1
	v_lshrrev_b32_e32 v13, 16, v13
	v_add3_u32 v15, v19, v15, s17
	v_and_or_b32 v15, v15, s18, v13
	global_store_dwordx2 v[28:29], v[14:15], off offset:96 sc1
	global_store_dwordx2 v[24:25], v[14:15], off offset:96 sc1

.LBB0_1454:
	s_and_b64 s[20:21], s[10:11], exec
	s_cselect_b32 s21, s27, s59
	s_cselect_b32 s20, s26, s58
	s_add_i32 s22, s14, 0xfffffc00
	s_and_b64 s[10:11], s[10:11], exec
	s_cselect_b32 s10, s14, s22
	v_lshl_add_u64 v[28:29], s[20:21], 0, v[2:3]
	s_ashr_i32 s11, s10, 31
	v_lshl_add_u64 v[28:29], s[10:11], 1, v[28:29]
	v_mov_b32_e32 v13, v3
	v_lshl_add_u64 v[28:29], v[28:29], 0, v[12:13]
	v_bfe_u32 v13, v32, 16, 1
	v_add3_u32 v13, v32, v13, s17
	v_bfe_u32 v32, v33, 16, 1
	v_lshrrev_b32_e32 v13, 16, v13
	v_add3_u32 v32, v33, v32, s17
	v_and_or_b32 v32, v32, s18, v13
	v_bfe_u32 v13, v30, 16, 1
	v_add3_u32 v13, v30, v13, s17
	v_bfe_u32 v30, v31, 16, 1
	v_lshrrev_b32_e32 v13, 16, v13
	v_add3_u32 v30, v31, v30, s17
	v_and_or_b32 v33, v30, s18, v13
	v_add_co_u32_e32 v30, vcc, 0x1020000, v28
	v_mov_b32_e32 v15, v14
	s_nop 0
	v_addc_co_u32_e32 v31, vcc, 0, v29, vcc
	global_store_dwordx2 v[30:31], v[32:33], off sc1
	v_mov_b32_e32 v30, v14
	v_mov_b32_e32 v31, v14
	global_store_dwordx2 v[28:29], v[32:33], off sc1
	v_pk_mul_f32 v[26:27], v[26:27], v[30:31]
	s_and_b64 vcc, exec, s[6:7]
	v_pk_mul_f32 v[32:33], v[24:25], v[14:15]
	s_cbranch_vccnz .LBB0_1456
	global_load_dwordx4 v[36:39], v[10:11], off offset:64
	s_waitcnt vmcnt(0)
	v_pk_mul_f32 v[26:27], v[26:27], v[38:39]
	v_pk_mul_f32 v[32:33], v[32:33], v[36:37]
.LBB0_1456:
	s_nop 0
	v_bfe_u32 v13, v32, 16, 1
	v_add3_u32 v13, v32, v13, s17
	v_bfe_u32 v32, v33, 16, 1
	v_lshrrev_b32_e32 v13, 16, v13
	v_add3_u32 v32, v33, v32, s17
	v_and_or_b32 v32, v32, s18, v13
	v_bfe_u32 v13, v26, 16, 1
	v_add3_u32 v13, v26, v13, s17
	v_bfe_u32 v26, v27, 16, 1
	v_lshrrev_b32_e32 v13, 16, v13
	v_add3_u32 v26, v27, v26, s17
	v_lshl_add_u64 v[24:25], v[28:29], 0, s[8:9]
	v_and_or_b32 v33, v26, s18, v13
	v_pk_mul_f32 v[22:23], v[22:23], v[30:31]
	s_and_b64 vcc, exec, s[6:7]
	v_pk_mul_f32 v[20:21], v[20:21], v[14:15]
	global_store_dwordx2 v[28:29], v[32:33], off offset:32 sc1
	global_store_dwordx2 v[24:25], v[32:33], off offset:32 sc1
	s_cbranch_vccnz .LBB0_1458
	global_load_dwordx4 v[30:33], v[10:11], off offset:128
	s_waitcnt vmcnt(0)
	v_pk_mul_f32 v[22:23], v[22:23], v[32:33]
	v_pk_mul_f32 v[20:21], v[20:21], v[30:31]
.LBB0_1458:
	s_nop 0
	v_bfe_u32 v13, v20, 16, 1
	v_add3_u32 v13, v20, v13, s17
	v_bfe_u32 v20, v21, 16, 1
	v_lshrrev_b32_e32 v13, 16, v13
	v_add3_u32 v20, v21, v20, s17
	v_and_or_b32 v20, v20, s18, v13
	v_bfe_u32 v13, v22, 16, 1
	v_add3_u32 v13, v22, v13, s17
	v_bfe_u32 v21, v23, 16, 1
	v_lshrrev_b32_e32 v13, 16, v13
	v_add3_u32 v21, v23, v21, s17
	v_and_or_b32 v21, v21, s18, v13
	global_store_dwordx2 v[28:29], v[20:21], off offset:64 sc1
	global_store_dwordx2 v[24:25], v[20:21], off offset:64 sc1
	v_mov_b32_e32 v20, v14
	v_mov_b32_e32 v21, v14
	v_pk_mul_f32 v[18:19], v[18:19], v[20:21]
	s_and_b64 vcc, exec, s[6:7]
	v_pk_mul_f32 v[14:15], v[16:17], v[14:15]
	s_cbranch_vccnz .LBB0_1447
	global_load_dwordx4 v[20:23], v[10:11], off offset:192
	s_waitcnt vmcnt(0)
	v_pk_mul_f32 v[18:19], v[18:19], v[22:23]
	v_pk_mul_f32 v[14:15], v[14:15], v[20:21]
	s_branch .LBB0_1447

.LBB0_1639:
	s_andn2_saveexec_b64 s[8:9], s[8:9]
	s_cbranch_execz .LBB0_1659
	s_mov_b64 s[8:9], exec
	s_waitcnt lgkmcnt(0)
	s_waitcnt vmcnt(0)
	v_mbcnt_lo_u32_b32 v2, s8, 0
	v_mbcnt_hi_u32_b32 v2, s9, v2
	v_cmp_eq_u32_e32 vcc, 0, v2
	s_and_saveexec_b64 s[10:11], vcc
	s_cbranch_execz .LBB0_1642
	s_bcnt1_i32_b64 s8, s[8:9]
	v_readlane_b32 s36, v253, 46
	v_mov_b32_e32 v3, 0x7000
	v_mov_b32_e32 v4, s8
	v_readlane_b32 s50, v253, 60
	v_readlane_b32 s51, v253, 61
	v_readlane_b32 s37, v253, 47
	v_readlane_b32 s38, v253, 48
	v_readlane_b32 s39, v253, 49
	v_readlane_b32 s40, v253, 50
	v_readlane_b32 s41, v253, 51
	global_atomic_add v3, v3, v4, s[50:51] offset:1024 sc0
	v_readlane_b32 s42, v253, 52
	v_readlane_b32 s43, v253, 53
	v_readlane_b32 s44, v253, 54
	v_readlane_b32 s45, v253, 55
	v_readlane_b32 s46, v253, 56
	v_readlane_b32 s47, v253, 57
	v_readlane_b32 s48, v253, 58
	v_readlane_b32 s49, v253, 59

.LBB0_1743:
	v_add_f32_e32 v35, v66, v67
	v_add_f32_e32 v35, v68, v35
	v_add_f32_e32 v35, v69, v35
	v_add_f32_e32 v35, v70, v35
	v_add_f32_e32 v35, v71, v35
	v_add_f32_e32 v35, v72, v35
	v_add_f32_e32 v35, v73, v35
	v_add_f32_e32 v35, v74, v35
	v_add_f32_e32 v35, v75, v35
	v_add_f32_e32 v35, v76, v35
	v_add_f32_e32 v35, v77, v35
	v_add_f32_e32 v35, v78, v35
	v_add_f32_e32 v35, v79, v35
	v_add_f32_e32 v35, v80, v35
	v_add_f32_e32 v35, v81, v35
	v_add_f32_e32 v35, v50, v35
	v_add_f32_e32 v35, v51, v35
	v_add_f32_e32 v35, v52, v35
	v_add_f32_e32 v35, v53, v35
	v_add_f32_e32 v35, v54, v35
	v_add_f32_e32 v35, v55, v35
	v_add_f32_e32 v35, v56, v35
	v_add_f32_e32 v35, v57, v35
	v_add_f32_e32 v35, v58, v35
	v_add_f32_e32 v35, v59, v35
	v_add_f32_e32 v35, v60, v35
	v_add_f32_e32 v35, v61, v35
	v_add_f32_e32 v35, v62, v35
	v_add_f32_e32 v35, v63, v35
	v_add_f32_e32 v35, v64, v35
	v_add_f32_e32 v35, v65, v35
	v_add_f32_e32 v34, v34, v35
	v_cvt_pk_bf16_f32 v36, v66, v67
	v_cvt_pk_bf16_f32 v37, v68, v69
	v_cvt_pk_bf16_f32 v38, v70, v71
	v_cvt_pk_bf16_f32 v39, v72, v73
	v_cvt_pk_bf16_f32 v40, v74, v75
	v_cvt_pk_bf16_f32 v41, v76, v77
	v_cvt_pk_bf16_f32 v42, v78, v79
	v_cvt_pk_bf16_f32 v43, v80, v81
	v_cvt_pk_bf16_f32 v44, v50, v51
	v_cvt_pk_bf16_f32 v45, v52, v53
	v_cvt_pk_bf16_f32 v46, v54, v55
	v_cvt_pk_bf16_f32 v47, v56, v57
	v_cvt_pk_bf16_f32 v48, v58, v59
	v_cvt_pk_bf16_f32 v49, v60, v61
	v_cvt_pk_bf16_f32 v50, v62, v63
	v_cvt_pk_bf16_f32 v51, v64, v65
	v_add_u32_e32 v35, s53, v234
	ds_read_b64_tr_b16 v[52:53],v35 offset:0
	ds_read_b64_tr_b16 v[54:55],v35 offset:512
	ds_read_b64_tr_b16 v[56:57],v35 offset:1024
	ds_read_b64_tr_b16 v[58:59],v35 offset:1536
	ds_read_b64_tr_b16 v[60:61],v35 offset:2048
	ds_read_b64_tr_b16 v[62:63],v35 offset:2560
	ds_read_b64_tr_b16 v[64:65],v35 offset:3072
	ds_read_b64_tr_b16 v[66:67],v35 offset:3584
	s_waitcnt lgkmcnt(0)
	s_nop 0
	v_mfma_f32_32x32x16_bf16 v[2:17], v[36:39], v[52:55], v[2:17]
	ds_read_b64_tr_b16 v[52:53],v35 offset:4096
	ds_read_b64_tr_b16 v[54:55],v35 offset:4608
	v_mfma_f32_32x32x16_bf16 v[2:17], v[40:43], v[56:59], v[2:17]
	ds_read_b64_tr_b16 v[56:57],v35 offset:5120
	ds_read_b64_tr_b16 v[58:59],v35 offset:5632
	v_mfma_f32_32x32x16_bf16 v[2:17], v[44:47], v[60:63], v[2:17]
	ds_read_b64_tr_b16 v[60:61],v35 offset:6144
	ds_read_b64_tr_b16 v[62:63],v35 offset:6656
	ds_read_b64_tr_b16 v[68:69],v35 offset:7168
	ds_read_b64_tr_b16 v[70:71],v35 offset:7680
	s_waitcnt lgkmcnt(0)
	v_mfma_f32_32x32x16_bf16 v[2:17], v[48:51], v[64:67], v[2:17]
	v_mfma_f32_32x32x16_bf16 v[18:33], v[36:39], v[52:55], v[18:33]
	s_cmp_eq_u64 s[36:37], 0
	v_mfma_f32_32x32x16_bf16 v[18:33], v[40:43], v[56:59], v[18:33]
	v_mfma_f32_32x32x16_bf16 v[18:33], v[44:47], v[60:63], v[18:33]
	v_mfma_f32_32x32x16_bf16 v[18:33], v[48:51], v[68:71], v[18:33]
	s_cbranch_scc1 .LBB0_1745
	s_mul_i32 s30, s48, 33
	s_lshl_b64 s[8:9], s[30:31], 8
	s_add_u32 s8, s36, s8
	v_and_b32_e32 v36, 63, v0
	s_addc_u32 s9, s37, s9
	v_lshlrev_b32_e32 v196, 2, v36
	v_lshl_add_u64 v[36:37], s[8:9], 0, v[196:197]
	v_add_co_u32_e32 v38, vcc, s46, v36
	global_store_dword v196, v2, s[8:9] sc1
	global_store_dword v196, v3, s[8:9] offset:256 sc1
	global_store_dword v196, v4, s[8:9] offset:512 sc1
	global_store_dword v196, v5, s[8:9] offset:768 sc1
	global_store_dword v196, v6, s[8:9] offset:1024 sc1
	global_store_dword v196, v7, s[8:9] offset:1280 sc1
	global_store_dword v196, v8, s[8:9] offset:1536 sc1
	global_store_dword v196, v9, s[8:9] offset:1792 sc1
	global_store_dword v196, v10, s[8:9] offset:2048 sc1
	global_store_dword v196, v11, s[8:9] offset:2304 sc1
	global_store_dword v196, v12, s[8:9] offset:2560 sc1
	global_store_dword v196, v13, s[8:9] offset:2816 sc1
	global_store_dword v196, v14, s[8:9] offset:3072 sc1
	global_store_dword v196, v15, s[8:9] offset:3328 sc1
	global_store_dword v196, v16, s[8:9] offset:3584 sc1
	global_store_dword v196, v17, s[8:9] offset:3840 sc1
	v_addc_co_u32_e32 v39, vcc, 0, v37, vcc
	v_add_co_u32_e32 v36, vcc, 0x2000, v36
	s_nop 1
	v_addc_co_u32_e32 v37, vcc, 0, v37, vcc
	global_store_dword v[38:39], v18, off sc1
	global_store_dword v[38:39], v19, off offset:256 sc1
	global_store_dword v[38:39], v20, off offset:512 sc1
	global_store_dword v[38:39], v21, off offset:768 sc1
	global_store_dword v[38:39], v22, off offset:1024 sc1
	global_store_dword v[38:39], v23, off offset:1280 sc1
	global_store_dword v[38:39], v24, off offset:1536 sc1
	global_store_dword v[38:39], v25, off offset:1792 sc1
	global_store_dword v[38:39], v26, off offset:2048 sc1
	global_store_dword v[38:39], v27, off offset:2304 sc1
	global_store_dword v[38:39], v28, off offset:2560 sc1
	global_store_dword v[38:39], v29, off offset:2816 sc1
	global_store_dword v[38:39], v30, off offset:3072 sc1
	global_store_dword v[38:39], v31, off offset:3328 sc1
	global_store_dword v[38:39], v32, off offset:3584 sc1
	global_store_dword v[38:39], v33, off offset:3840 sc1
	global_store_dword v[36:37], v34, off sc1
	s_cbranch_execnz .LBB0_1749
	s_branch .LBB0_1746

.LBB0_1782:
	s_andn2_saveexec_b64 s[10:11], s[10:11]
	s_cbranch_execz .LBB0_1802
	s_mov_b64 s[10:11], exec
	s_waitcnt lgkmcnt(0)
	s_waitcnt vmcnt(0)
	v_mbcnt_lo_u32_b32 v3, s10, 0
	v_mbcnt_hi_u32_b32 v3, s11, v3
	v_cmp_eq_u32_e32 vcc, 0, v3
	s_and_saveexec_b64 s[12:13], vcc
	s_cbranch_execz .LBB0_1785
	s_bcnt1_i32_b64 s10, s[10:11]
	v_mov_b32_e32 v4, 0x7000
	v_mov_b32_e32 v5, s10
	global_atomic_add v4, v4, v5, s[54:55] offset:1024 sc0

.LBB0_1844:
	s_andn2_saveexec_b64 s[8:9], s[8:9]
	s_cbranch_execz .LBB0_1864
	s_mov_b64 s[8:9], exec
	s_waitcnt lgkmcnt(0)
	s_waitcnt vmcnt(0)
	v_mbcnt_lo_u32_b32 v2, s8, 0
	v_mbcnt_hi_u32_b32 v2, s9, v2
	v_cmp_eq_u32_e32 vcc, 0, v2
	s_and_saveexec_b64 s[10:11], vcc
	s_cbranch_execz .LBB0_1847
	s_bcnt1_i32_b64 s8, s[8:9]
	v_mov_b32_e32 v3, 0x7000
	v_mov_b32_e32 v4, s8
	global_atomic_add v3, v3, v4, s[50:51] offset:1024 sc0

.LBB0_1923:
	s_andn2_saveexec_b64 s[6:7], s[6:7]
	s_cbranch_execz .LBB0_1943
	s_mov_b64 s[6:7], exec
	s_waitcnt lgkmcnt(0)
	s_waitcnt vmcnt(0)
	v_mbcnt_lo_u32_b32 v2, s6, 0
	v_mbcnt_hi_u32_b32 v2, s7, v2
	v_cmp_eq_u32_e32 vcc, 0, v2
	s_and_saveexec_b64 s[8:9], vcc
	s_cbranch_execz .LBB0_1926
	s_bcnt1_i32_b64 s6, s[6:7]
	v_mov_b32_e32 v3, 0x7000
	v_mov_b32_e32 v4, s6
	global_atomic_add v3, v3, v4, s[50:51] offset:1024 sc0

.LBB0_1987:
	s_or_b64 exec, exec, s[2:3]
	s_waitcnt lgkmcnt(0)
	s_barrier
	s_and_saveexec_b64 s[2:3], s[4:5]
	s_cbranch_execz .LBB0_1990
	v_lshl_add_u32 v1, v0, 2, 0
	v_add_u32_e32 v1, 0x1ee80, v1
	ds_read_b32 v1, v1
	s_waitcnt lgkmcnt(0)
	v_cmp_lt_i32_e32 vcc, -1, v1
	s_and_b64 exec, exec, vcc
	s_cbranch_execz .LBB0_1990
	v_bfe_u32 v2, v1, 8, 8
	v_mul_u32_u24_e32 v6, 0x4010, v2
	v_lshl_add_u32 v2, v2, 2, 0
	v_add_u32_e32 v2, 0x1ee00, v2
	ds_read_b32 v7, v2
	v_lshl_add_u32 v2, v0, 4, 0
	v_add_u32_e32 v2, 0x1f180, v2
	ds_read_b128 v[2:5], v2
	v_and_b32_e32 v8, 0xff, v1
	s_waitcnt lgkmcnt(1)
	v_add3_u32 v6, v6, v8, v7
	v_ashrrev_i32_e32 v7, 31, v6
	v_lshrrev_b32_e32 v1, 16, v1
	v_lshl_add_u64 v[8:9], v[6:7], 2, s[24:25]
	v_lshl_add_u64 v[6:7], v[6:7], 4, s[28:29]
	global_store_dword v[8:9], v1, off sc1
	s_waitcnt lgkmcnt(0)
	global_store_dwordx4 v[6:7], v[2:5], off sc1
